# parallel counter loads in MoE prefix setup; hoisted partial loads in merge epilogues; head-major int8 partial layout
# speedup vs baseline: 1.0123x; 1.0123x over previous
.LBB0_514:
	s_ashr_i32 s0, s55, 10
	s_lshl_b32 s1, s0, 25
	s_lshl_b32 s0, s0, 18
	v_add_u32_e32 v4, s78, v206
	v_lshl_add_u32 v5, v4, 3, s0
	s_lshl_b32 s0, s78, 10
	s_or_b32 s0, s0, s1
	s_lshl_b32 s1, s59, 20
	s_or_b32 s0, s0, s1
	v_lshl_add_u32 v4, v206, 7, s0
	v_or_b32_e32 v6, s59, v5
	v_cmp_lt_i32_e64 s[6:7], -1, v4
	v_cmp_gt_u32_e64 s[8:9], 32, v205
	v_cmp_lt_f32_e32 vcc, 0, v3
	s_and_b64 s[76:77], s[6:7], s[8:9]
	v_ashrrev_i32_e32 v7, 31, v6
	s_and_saveexec_b64 s[78:79], s[76:77]
	v_readlane_b32 s92, v255, 35
	v_readlane_b32 s90, v255, 33
	v_readlane_b32 s93, v255, 36
	v_readlane_b32 s94, v255, 37
	v_readlane_b32 s91, v255, 34
	v_readlane_b32 s95, v255, 38
	s_cbranch_execz .LBB0_516
	s_mov_b32 s0, 0x800000
	v_cmp_gt_f32_e64 s[8:9], s0, v3
	v_readlane_b32 s0, v255, 27
	v_readlane_b32 s1, v255, 28
	v_cndmask_b32_e64 v8, 0, 32, s[8:9]
	v_ldexp_f32 v8, v3, v8
	v_log_f32_e32 v10, v8
	v_cndmask_b32_e64 v5, 0, v177, s[8:9]
	v_lshl_add_u64 v[8:9], v[6:7], 2, s[0:1]
	v_sub_f32_e32 v5, v10, v5
	v_add_f32_e32 v5, v207, v5
	v_cndmask_b32_e32 v5, v175, v5, vcc
	global_store_dword v[8:9], v5, off

.LBB0_572:
	v_add_f32_e32 v86, v196, v197
	v_add_f32_e32 v86, v86, v198
	v_add_f32_e32 v87, v202, v203
	v_fmac_f32_e32 v87, v86, v170
	v_add_f32_e32 v86, v204, v205
	v_fmac_f32_e32 v86, v87, v172
	v_add_f32_e32 v84, v84, v85
	v_fmac_f32_e32 v84, v86, v82
	ds_read_b64_tr_b16 v[86:87], v171 offset:0xc000
	ds_read_b64_tr_b16 v[88:89], v171 offset:0xc800
	ds_read_b64_tr_b16 v[90:91], v171 offset:0xd000
	ds_read_b64_tr_b16 v[92:93], v171 offset:0xd800
	ds_read_b64_tr_b16 v[94:95], v171 offset:0xe000
	ds_read_b64_tr_b16 v[96:97], v171 offset:0xe800
	ds_read_b64_tr_b16 v[130:131], v171 offset:0xf000
	ds_read_b64_tr_b16 v[132:133], v171 offset:0xf800
	s_waitcnt lgkmcnt(0)
	s_nop 0
	v_mfma_f32_32x32x16_bf16 v[18:33], v[86:89], v[74:77], v[18:33]
	ds_read_b64_tr_b16 v[86:87], v171 offset:0xc200
	ds_read_b64_tr_b16 v[88:89], v171 offset:0xca00
	v_mfma_f32_32x32x16_bf16 v[18:33], v[90:93], v[78:81], v[18:33]
	ds_read_b64_tr_b16 v[90:91], v171 offset:0xd200
	ds_read_b64_tr_b16 v[92:93], v171 offset:0xda00
	v_mfma_f32_32x32x16_bf16 v[18:33], v[94:97], v[70:73], v[18:33]
	ds_read_b64_tr_b16 v[94:95], v171 offset:0xe200
	ds_read_b64_tr_b16 v[96:97], v171 offset:0xea00
	ds_read_b64_tr_b16 v[134:135], v171 offset:0xf200
	ds_read_b64_tr_b16 v[136:137], v171 offset:0xfa00
	s_waitcnt lgkmcnt(0)
	v_mfma_f32_32x32x16_bf16 v[18:33], v[130:133], v[66:69], v[18:33]
	v_mfma_f32_32x32x16_bf16 v[34:49], v[86:89], v[74:77], v[34:49]
	ds_read_b64_tr_b16 v[86:87], v171 offset:0xc400
	ds_read_b64_tr_b16 v[88:89], v171 offset:0xcc00
	v_mfma_f32_32x32x16_bf16 v[34:49], v[90:93], v[78:81], v[34:49]
	ds_read_b64_tr_b16 v[90:91], v171 offset:0xd400
	ds_read_b64_tr_b16 v[92:93], v171 offset:0xdc00
	v_mfma_f32_32x32x16_bf16 v[34:49], v[94:97], v[70:73], v[34:49]
	ds_read_b64_tr_b16 v[94:95], v171 offset:0xe400
	ds_read_b64_tr_b16 v[96:97], v171 offset:0xec00
	ds_read_b64_tr_b16 v[130:131], v171 offset:0xf400
	ds_read_b64_tr_b16 v[132:133], v171 offset:0xfc00
	s_waitcnt lgkmcnt(0)
	v_mfma_f32_32x32x16_bf16 v[34:49], v[134:137], v[66:69], v[34:49]
	v_mfma_f32_32x32x16_bf16 v[50:65], v[86:89], v[74:77], v[50:65]
	ds_read_b64_tr_b16 v[86:87], v171 offset:0xc600
	ds_read_b64_tr_b16 v[88:89], v171 offset:0xce00
	v_mfma_f32_32x32x16_bf16 v[50:65], v[90:93], v[78:81], v[50:65]
	ds_read_b64_tr_b16 v[90:91], v171 offset:0xd600
	ds_read_b64_tr_b16 v[92:93], v171 offset:0xde00
	v_mfma_f32_32x32x16_bf16 v[50:65], v[94:97], v[70:73], v[50:65]
	ds_read_b64_tr_b16 v[94:95], v171 offset:0xe600
	ds_read_b64_tr_b16 v[96:97], v171 offset:0xee00
	ds_read_b64_tr_b16 v[134:135], v171 offset:0xf600
	ds_read_b64_tr_b16 v[136:137], v171 offset:0xfe00
	s_waitcnt lgkmcnt(0)
	v_mfma_f32_32x32x16_bf16 v[50:65], v[130:133], v[66:69], v[50:65]
	v_mfma_f32_32x32x16_bf16 v[2:17], v[86:89], v[74:77], v[2:17]
	v_lshlrev_b32_sdwa v74, v188, v195 dst_sel:DWORD dst_unused:UNUSED_PAD src0_sel:DWORD src1_sel:WORD_1
	v_lshlrev_b32_e32 v75, 7, v194
	s_bfe_u32 vcc_lo, s20, 0x30007
	s_lshl_b32 vcc_lo, vcc_lo, 20
	s_and_b32 vcc_hi, s20, 0xff800000
	s_or_b32 vcc_lo, vcc_lo, vcc_hi
	v_add3_u32 v74, v74, v75, vcc_lo
	v_ashrrev_i32_e32 v75, 31, v74
	v_cndmask_b32_e64 v74, -1, v74, s[12:13]
	v_cndmask_b32_e64 v75, -1, v75, s[12:13]
	v_cmp_lt_i64_e64 s[10:11], -1, v[74:75]
	v_mfma_f32_32x32x16_bf16 v[2:17], v[90:93], v[78:81], v[2:17]
	v_cmp_lt_f32_e32 vcc, 0, v84
	s_and_b64 s[66:67], s[8:9], s[10:11]
	v_mfma_f32_32x32x16_bf16 v[2:17], v[94:97], v[70:73], v[2:17]
	v_lshlrev_b32_sdwa v70, v189, v195 dst_sel:DWORD dst_unused:UNUSED_PAD src0_sel:DWORD src1_sel:WORD_1
	v_add_u32_e32 v71, s1, v194
	v_lshl_add_u32 v70, v71, 3, v70
	v_or_b32_e32 v70, s0, v70
	v_ashrrev_i32_e32 v71, 31, v70
	v_mfma_f32_32x32x16_bf16 v[2:17], v[134:137], v[66:69], v[2:17]
	s_and_saveexec_b64 s[68:69], s[66:67]
	s_cbranch_execz .LBB0_574
	v_cmp_gt_f32_e64 s[12:13], s49, v84
	v_readlane_b32 s0, v255, 25
	v_readlane_b32 s1, v255, 26
	v_cndmask_b32_e64 v66, 0, 32, s[12:13]
	v_ldexp_f32 v66, v84, v66
	v_log_f32_e32 v69, v66
	v_cndmask_b32_e64 v68, 0, v190, s[12:13]
	v_lshl_add_u64 v[66:67], v[70:71], 2, s[0:1]
	v_sub_f32_e32 v68, v69, v68
	v_add_f32_e32 v68, v83, v68
	v_cndmask_b32_e32 v68, v191, v68, vcc
	global_store_dword v[66:67], v68, off

.LBB0_691:
	v_cmp_lt_i32_e64 s[74:75], -1, v182
	v_readlane_b32 s10, v255, 27
	v_readlane_b32 s11, v255, 28
	v_readlane_b32 s20, v255, 50
	v_readlane_b32 s21, v255, 51
	v_cndmask_b32_e64 v230, 0, v225, s[74:75]
	v_ashrrev_i32_e32 v231, 31, v230
	v_lshl_add_u64 v[240:241], v[230:231], 2, s[10:11]
	global_load_dword v162, v[240:241], off
	v_lshl_add_u64 v[240:241], v[230:231], 2, s[20:21]
	global_load_dword v163, v[240:241], off
	v_readlane_b32 s10, v255, 31
	v_readlane_b32 s11, v255, 32
	v_readlane_b32 s20, v255, 52
	v_readlane_b32 s21, v255, 53
	v_lshrrev_b32_e32 v234, 4, v254
	v_and_b32_e32 v235, 15, v254
	v_lshl_add_u64 v[240:241], v[230:231], 2, s[10:11]
	global_load_dword v164, v[240:241], off
	v_lshl_add_u64 v[240:241], v[230:231], 2, s[20:21]
	global_load_dword v165, v[240:241], off
	v_readlane_b32 s10, v255, 23
	v_readlane_b32 s11, v255, 24
	v_readlane_b32 s20, v255, 39
	v_readlane_b32 s21, v255, 40
	v_and_b32_e32 v240, 0xff800000, v182
	v_bfe_u32 v241, v182, 7, 3
	v_lshl_or_b32 v240, v241, 20, v240
	v_bfe_u32 v241, v182, 10, 13
	v_lshl_or_b32 v240, v241, 7, v240
	s_nop 0
	v_readfirstlane_b32 vcc_lo, v240
	v_readlane_b32 vcc_hi, v255, 2
	v_lshlrev_b32_e32 v235, 3, v235
	v_mul_u32_u24_e32 v232, 0x800, v234
	v_add_u32_e32 v232, v232, v235
	v_mul_u32_u24_e32 v233, 0x88, v234
	v_add_u32_e32 v233, v233, v235
	v_and_b32_e32 v236, 31, v254
	v_lshrrev_b32_e32 v237, 5, v254
	v_lshlrev_b32_e32 v237, 3, v237
	v_mul_u32_u24_e32 v236, 0x88, v236
	v_add_u32_e32 v236, v236, v237
	s_mul_i32 vcc_hi, vcc_hi, 0x2400
	s_add_u32 vcc_hi, vcc_hi, 0x10000
	s_add_u32 s10, s10, vcc_lo
	s_addc_u32 s11, s11, 0
	s_add_u32 s20, s20, vcc_lo
	s_addc_u32 s21, s21, 0
	v_add_u32_e32 v233, vcc_hi, v233
	v_add_u32_e32 v236, vcc_hi, v236
	global_load_dwordx2 v[166:167], v232, s[10:11]
	s_add_u32 s10, s10, 0x2000
	s_addc_u32 s11, s11, 0
	global_load_dwordx2 v[168:169], v232, s[10:11]
	s_add_u32 s10, s10, 0x2000
	s_addc_u32 s11, s11, 0
	global_load_dwordx2 v[170:171], v232, s[10:11]
	s_add_u32 s10, s10, 0x2000
	s_addc_u32 s11, s11, 0
	global_load_dwordx2 v[172:173], v232, s[10:11]
	s_add_u32 s10, s10, 0x2000
	s_addc_u32 s11, s11, 0
	global_load_dwordx2 v[174:175], v232, s[10:11]
	s_add_u32 s10, s10, 0x2000
	s_addc_u32 s11, s11, 0
	global_load_dwordx2 v[176:177], v232, s[10:11]
	s_add_u32 s10, s10, 0x2000
	s_addc_u32 s11, s11, 0
	global_load_dwordx2 v[200:201], v232, s[10:11]
	s_add_u32 s10, s10, 0x2000
	s_addc_u32 s11, s11, 0
	global_load_dwordx2 v[202:203], v232, s[10:11]
	global_load_dwordx2 v[204:205], v232, s[20:21]
	s_add_u32 s20, s20, 0x2000
	s_addc_u32 s21, s21, 0
	global_load_dwordx2 v[206:207], v232, s[20:21]
	s_add_u32 s20, s20, 0x2000
	s_addc_u32 s21, s21, 0
	global_load_dwordx2 v[208:209], v232, s[20:21]
	s_add_u32 s20, s20, 0x2000
	s_addc_u32 s21, s21, 0
	global_load_dwordx2 v[210:211], v232, s[20:21]
	s_add_u32 s20, s20, 0x2000
	s_addc_u32 s21, s21, 0
	global_load_dwordx2 v[212:213], v232, s[20:21]
	s_add_u32 s20, s20, 0x2000
	s_addc_u32 s21, s21, 0
	global_load_dwordx2 v[214:215], v232, s[20:21]
	s_add_u32 s20, s20, 0x2000
	s_addc_u32 s21, s21, 0
	global_load_dwordx2 v[216:217], v232, s[20:21]
	s_add_u32 s20, s20, 0x2000
	s_addc_u32 s21, s21, 0
	global_load_dwordx2 v[218:219], v232, s[20:21]
	v_cmp_lt_i32_e64 s[74:75], -1, v182
	s_cmp_eq_u32 s93, 0
	v_mov_b32_e32 v16, 0xff800000
	v_cmp_lt_f32_e64 s[8:9], 0, v244
	v_cndmask_b32_e64 v104, 0, v225, s[74:75]
	s_cselect_b64 s[6:7], -1, 0
	s_cmp_lg_u32 s93, 0
	v_cndmask_b32_e64 v17, v16, v183, s[8:9]
	v_ashrrev_i32_e32 v105, 31, v104
	s_cselect_b64 s[56:57], -1, 0
	s_and_b64 vcc, exec, s[6:7]
	s_cbranch_vccnz .LBB0_693
	v_readlane_b32 s10, v255, 27
	v_readlane_b32 s11, v255, 28
	v_max_f32_e32 v17, v17, v17
	s_nop 0
	v_lshl_add_u64 v[102:103], v[104:105], 2, s[10:11]
	s_waitcnt vmcnt(0)
	ds_write_b64 v233, v[166:167]
	ds_write_b64 v233, v[168:169] offset:544
	ds_write_b64 v233, v[170:171] offset:1088
	ds_write_b64 v233, v[172:173] offset:1632
	ds_write_b64 v233, v[174:175] offset:2176
	ds_write_b64 v233, v[176:177] offset:2720
	ds_write_b64 v233, v[200:201] offset:3264
	ds_write_b64 v233, v[202:203] offset:3808
	ds_write_b64 v233, v[204:205] offset:4352
	ds_write_b64 v233, v[206:207] offset:4896
	ds_write_b64 v233, v[208:209] offset:5440
	ds_write_b64 v233, v[210:211] offset:5984
	ds_write_b64 v233, v[212:213] offset:6528
	ds_write_b64 v233, v[214:215] offset:7072
	ds_write_b64 v233, v[216:217] offset:7616
	ds_write_b64 v233, v[218:219] offset:8160
	ds_read_b64 v[166:167], v236
	ds_read_b64 v[168:169], v236 offset:16
	ds_read_b64 v[170:171], v236 offset:32
	ds_read_b64 v[172:173], v236 offset:48
	ds_read_b64 v[174:175], v236 offset:64
	ds_read_b64 v[176:177], v236 offset:80
	ds_read_b64 v[200:201], v236 offset:96
	ds_read_b64 v[202:203], v236 offset:112
	ds_read_b64 v[204:205], v236 offset:4352
	ds_read_b64 v[206:207], v236 offset:4368
	ds_read_b64 v[208:209], v236 offset:4384
	ds_read_b64 v[210:211], v236 offset:4400
	ds_read_b64 v[212:213], v236 offset:4416
	ds_read_b64 v[214:215], v236 offset:4432
	ds_read_b64 v[216:217], v236 offset:4448
	ds_read_b64 v[218:219], v236 offset:4464
	s_waitcnt lgkmcnt(0)
	v_mov_b32_e32 v102, v162
	v_max_f32_e32 v3, v102, v102
	v_max_f32_e32 v17, v17, v3
	s_cmp_gt_u32 s93, 1
	s_cselect_b64 s[10:11], -1, 0
	s_cmp_lt_u32 s93, 2
	s_cbranch_scc0 .LBB0_694
	s_branch .LBB0_695

.LBB0_694:
	v_readlane_b32 s20, v255, 50
	v_readlane_b32 s21, v255, 51
	v_max_f32_e32 v17, v17, v17
	s_nop 0
	v_lshl_add_u64 v[106:107], v[104:105], 2, s[20:21]
	v_mov_b32_e32 v16, v163
	v_max_f32_e32 v3, v16, v16
	v_max_f32_e32 v17, v17, v3
.LBB0_695:
	v_sub_f32_e32 v3, v183, v17
	v_sub_f32_e32 v103, v102, v17
	v_exp_f32_e32 v3, v3
	v_exp_f32_e32 v103, v103
	v_sub_f32_e32 v17, v16, v17
	v_exp_f32_e32 v17, v17
	v_cmp_lg_f32_e32 vcc, s48, v102
	v_cndmask_b32_e64 v3, 0, v3, s[8:9]
	v_mul_f32_e32 v106, v244, v3
	v_cndmask_b32_e32 v102, 0, v103, vcc
	v_cndmask_b32_e64 v103, v102, 0, s[6:7]
	v_fmac_f32_e32 v102, v244, v3
	v_cmp_lg_f32_e32 vcc, s48, v16
	v_cndmask_b32_e64 v102, v102, v106, s[6:7]
	s_nop 0
	v_cndmask_b32_e32 v16, 0, v17, vcc
	v_add_f32_e32 v17, v16, v102
	v_cndmask_b32_e64 v102, v102, v17, s[10:11]
	v_div_scale_f32 v106, s[6:7], v102, v102, 1.0
	v_rcp_f32_e32 v107, v106
	v_cndmask_b32_e64 v17, 0, v16, s[10:11]
	v_fma_f32 v16, -v106, v107, 1.0
	v_fmac_f32_e32 v107, v16, v107
	v_div_scale_f32 v16, vcc, 1.0, v102, 1.0
	v_mul_f32_e32 v108, v16, v107
	v_fma_f32 v109, -v106, v108, v16
	v_fmac_f32_e32 v108, v109, v107
	v_fma_f32 v16, -v106, v108, v16
	v_div_fmas_f32 v16, v16, v107, v108
	v_div_fixup_f32 v16, v16, v102, 1.0
	v_cmp_lt_f32_e32 vcc, 0, v102
	v_cndmask_b32_e64 v102, 0, 1, s[56:57]
	v_cmp_ne_u32_e64 s[8:9], 1, v102
	v_cndmask_b32_e32 v106, 0, v16, vcc
	v_mov_b32_e32 v16, 0
	s_andn2_b64 vcc, exec, s[56:57]
	v_mov_b32_e32 v102, 0
	s_cbranch_vccnz .LBB0_697
	v_readlane_b32 s6, v255, 31
	v_readlane_b32 s7, v255, 32
	v_mul_f32_e32 v103, v103, v106
	s_nop 0
	v_lshl_add_u64 v[108:109], v[104:105], 2, s[6:7]
	v_mov_b32_e32 v102, v164
	v_mul_f32_e32 v102, v103, v102
.LBB0_697:
	v_cndmask_b32_e64 v103, 0, 1, s[10:11]
	v_cmp_ne_u32_e64 s[6:7], 1, v103
	s_andn2_b64 vcc, exec, s[10:11]
	s_cbranch_vccnz .LBB0_699
	v_readlane_b32 s10, v255, 52
	v_readlane_b32 s11, v255, 53
	v_mul_f32_e32 v17, v17, v106
	s_nop 0
	v_lshl_add_u64 v[104:105], v[104:105], 2, s[10:11]
	v_mov_b32_e32 v16, v165
	v_mul_f32_e32 v16, v17, v16
.LBB0_699:
	v_ashrrev_i32_e32 v183, 31, v182
	v_readlane_b32 s10, v255, 23
	s_waitcnt vmcnt(0)
	v_cndmask_b32_e64 v179, 0, v183, s[74:75]
	v_cndmask_b32_e64 v178, 0, v182, s[74:75]
	v_mul_f32_e32 v104, v3, v106
	v_lshlrev_b32_e32 v108, 3, v199
	v_readlane_b32 s11, v255, 24
	v_ashrrev_i32_e32 v109, 31, v108
	v_pk_mul_f32 v[110:111], v[70:71], v[104:105] op_sel_hi:[1,0]
	v_lshl_add_u64 v[70:71], s[10:11], 0, v[178:179]
	v_pk_mul_f32 v[66:67], v[66:67], v[104:105] op_sel_hi:[1,0]
	v_pk_mul_f32 v[68:69], v[68:69], v[104:105] op_sel_hi:[1,0]
	v_pk_mul_f32 v[112:113], v[72:73], v[104:105] op_sel_hi:[1,0]
	v_pk_mul_f32 v[106:107], v[74:75], v[104:105] op_sel_hi:[1,0]
	v_pk_mul_f32 v[76:77], v[76:77], v[104:105] op_sel_hi:[1,0]
	v_pk_mul_f32 v[78:79], v[78:79], v[104:105] op_sel_hi:[1,0]
	v_pk_mul_f32 v[80:81], v[80:81], v[104:105] op_sel_hi:[1,0]
	s_and_b64 vcc, exec, s[8:9]
	v_lshl_add_u64 v[72:73], v[70:71], 0, v[108:109]
	s_cbranch_vccnz .LBB0_701
	v_mov_b32_e32 v70, v166
	v_mov_b32_e32 v3, v167
	v_mov_b32_e32 v74, v168
	v_mov_b32_e32 v17, v169
	v_permlane32_swap_b32_e32 v70, v3
	s_nop 0
	v_permlane32_swap_b32_e32 v74, v17
	v_cvt_f32_i32_sdwa v181, sext(v70) dst_sel:DWORD dst_unused:UNUSED_PAD src0_sel:BYTE_1
	v_cvt_f32_i32_sdwa v180, sext(v70) dst_sel:DWORD dst_unused:UNUSED_PAD src0_sel:BYTE_0
	v_cvt_f32_i32_sdwa v71, sext(v70) dst_sel:DWORD dst_unused:UNUSED_PAD src0_sel:BYTE_3
	v_cvt_f32_i32_sdwa v70, sext(v70) dst_sel:DWORD dst_unused:UNUSED_PAD src0_sel:BYTE_2
	v_cvt_f32_i32_sdwa v187, sext(v3) dst_sel:DWORD dst_unused:UNUSED_PAD src0_sel:BYTE_1
	v_cvt_f32_i32_sdwa v186, sext(v3) dst_sel:DWORD dst_unused:UNUSED_PAD src0_sel:BYTE_0
	v_cvt_f32_i32_sdwa v189, sext(v3) dst_sel:DWORD dst_unused:UNUSED_PAD src0_sel:BYTE_3
	v_cvt_f32_i32_sdwa v188, sext(v3) dst_sel:DWORD dst_unused:UNUSED_PAD src0_sel:BYTE_2
	v_cvt_f32_i32_sdwa v191, sext(v74) dst_sel:DWORD dst_unused:UNUSED_PAD src0_sel:BYTE_1
	v_cvt_f32_i32_sdwa v190, sext(v74) dst_sel:DWORD dst_unused:UNUSED_PAD src0_sel:BYTE_0
	v_cvt_f32_i32_sdwa v75, sext(v74) dst_sel:DWORD dst_unused:UNUSED_PAD src0_sel:BYTE_3
	v_cvt_f32_i32_sdwa v74, sext(v74) dst_sel:DWORD dst_unused:UNUSED_PAD src0_sel:BYTE_2
	v_cvt_f32_i32_sdwa v193, sext(v17) dst_sel:DWORD dst_unused:UNUSED_PAD src0_sel:BYTE_1
	v_cvt_f32_i32_sdwa v192, sext(v17) dst_sel:DWORD dst_unused:UNUSED_PAD src0_sel:BYTE_0
	v_cvt_f32_i32_sdwa v197, sext(v17) dst_sel:DWORD dst_unused:UNUSED_PAD src0_sel:BYTE_3
	v_cvt_f32_i32_sdwa v196, sext(v17) dst_sel:DWORD dst_unused:UNUSED_PAD src0_sel:BYTE_2
	v_pk_fma_f32 v[76:77], v[102:103], v[74:75], v[76:77] op_sel_hi:[0,1,1]
	v_pk_fma_f32 v[78:79], v[102:103], v[192:193], v[78:79] op_sel_hi:[0,1,1]
	v_pk_fma_f32 v[106:107], v[102:103], v[190:191], v[106:107] op_sel_hi:[0,1,1]
	v_pk_fma_f32 v[80:81], v[102:103], v[196:197], v[80:81] op_sel_hi:[0,1,1]
	v_pk_fma_f32 v[112:113], v[102:103], v[188:189], v[112:113] op_sel_hi:[0,1,1]
	v_pk_fma_f32 v[110:111], v[102:103], v[186:187], v[110:111] op_sel_hi:[0,1,1]
	v_pk_fma_f32 v[68:69], v[102:103], v[70:71], v[68:69] op_sel_hi:[0,1,1]
	v_pk_fma_f32 v[66:67], v[102:103], v[180:181], v[66:67] op_sel_hi:[0,1,1]
.LBB0_701:
	v_readlane_b32 s10, v255, 39
	v_readlane_b32 s11, v255, 40
	s_and_b64 vcc, exec, s[6:7]
	s_nop 0
	v_lshl_add_u64 v[70:71], s[10:11], 0, v[178:179]
	v_lshl_add_u64 v[74:75], v[70:71], 0, v[108:109]
	s_cbranch_vccnz .LBB0_703
	v_mov_b32_e32 v70, v204
	v_mov_b32_e32 v3, v205
	v_mov_b32_e32 v178, v206
	v_mov_b32_e32 v17, v207
	v_permlane32_swap_b32_e32 v70, v3
	s_nop 0
	v_permlane32_swap_b32_e32 v178, v17
	v_cvt_f32_i32_sdwa v181, sext(v70) dst_sel:DWORD dst_unused:UNUSED_PAD src0_sel:BYTE_1
	v_cvt_f32_i32_sdwa v180, sext(v70) dst_sel:DWORD dst_unused:UNUSED_PAD src0_sel:BYTE_0
	v_cvt_f32_i32_sdwa v71, sext(v70) dst_sel:DWORD dst_unused:UNUSED_PAD src0_sel:BYTE_3
	v_cvt_f32_i32_sdwa v70, sext(v70) dst_sel:DWORD dst_unused:UNUSED_PAD src0_sel:BYTE_2
	v_cvt_f32_i32_sdwa v187, sext(v3) dst_sel:DWORD dst_unused:UNUSED_PAD src0_sel:BYTE_1
	v_cvt_f32_i32_sdwa v186, sext(v3) dst_sel:DWORD dst_unused:UNUSED_PAD src0_sel:BYTE_0
	v_cvt_f32_i32_sdwa v189, sext(v3) dst_sel:DWORD dst_unused:UNUSED_PAD src0_sel:BYTE_3
	v_cvt_f32_i32_sdwa v188, sext(v3) dst_sel:DWORD dst_unused:UNUSED_PAD src0_sel:BYTE_2
	v_cvt_f32_i32_sdwa v191, sext(v178) dst_sel:DWORD dst_unused:UNUSED_PAD src0_sel:BYTE_1
	v_cvt_f32_i32_sdwa v190, sext(v178) dst_sel:DWORD dst_unused:UNUSED_PAD src0_sel:BYTE_0
	v_cvt_f32_i32_sdwa v179, sext(v178) dst_sel:DWORD dst_unused:UNUSED_PAD src0_sel:BYTE_3
	v_cvt_f32_i32_sdwa v178, sext(v178) dst_sel:DWORD dst_unused:UNUSED_PAD src0_sel:BYTE_2
	v_cvt_f32_i32_sdwa v193, sext(v17) dst_sel:DWORD dst_unused:UNUSED_PAD src0_sel:BYTE_1
	v_cvt_f32_i32_sdwa v192, sext(v17) dst_sel:DWORD dst_unused:UNUSED_PAD src0_sel:BYTE_0
	v_cvt_f32_i32_sdwa v197, sext(v17) dst_sel:DWORD dst_unused:UNUSED_PAD src0_sel:BYTE_3
	v_cvt_f32_i32_sdwa v196, sext(v17) dst_sel:DWORD dst_unused:UNUSED_PAD src0_sel:BYTE_2
	v_pk_fma_f32 v[76:77], v[16:17], v[178:179], v[76:77] op_sel_hi:[0,1,1]
	v_pk_fma_f32 v[78:79], v[16:17], v[192:193], v[78:79] op_sel_hi:[0,1,1]
	v_pk_fma_f32 v[106:107], v[16:17], v[190:191], v[106:107] op_sel_hi:[0,1,1]
	v_pk_fma_f32 v[80:81], v[16:17], v[196:197], v[80:81] op_sel_hi:[0,1,1]
	v_pk_fma_f32 v[112:113], v[16:17], v[188:189], v[112:113] op_sel_hi:[0,1,1]
	v_pk_fma_f32 v[110:111], v[16:17], v[186:187], v[110:111] op_sel_hi:[0,1,1]
	v_pk_fma_f32 v[68:69], v[16:17], v[70:71], v[68:69] op_sel_hi:[0,1,1]
	v_pk_fma_f32 v[66:67], v[16:17], v[180:181], v[66:67] op_sel_hi:[0,1,1]

.LBB0_707:
	s_or_b64 exec, exec, s[10:11]
	v_mov_b32_e32 v105, v104
	v_pk_mul_f32 v[50:51], v[50:51], v[104:105]
	v_pk_mul_f32 v[52:53], v[52:53], v[104:105]
	v_pk_mul_f32 v[66:67], v[54:55], v[104:105]
	v_pk_mul_f32 v[68:69], v[56:57], v[104:105]
	v_pk_mul_f32 v[54:55], v[58:59], v[104:105]
	v_pk_mul_f32 v[56:57], v[60:61], v[104:105]
	v_pk_mul_f32 v[58:59], v[62:63], v[104:105]
	s_and_b64 vcc, exec, s[8:9]
	v_pk_mul_f32 v[60:61], v[64:65], v[104:105]
	s_cbranch_vccnz .LBB0_709
	v_mov_b32_e32 v62, v170
	v_mov_b32_e32 v3, v171
	v_mov_b32_e32 v64, v172
	v_mov_b32_e32 v17, v173
	v_permlane32_swap_b32_e32 v62, v3
	s_nop 0
	v_permlane32_swap_b32_e32 v64, v17
	v_cvt_f32_i32_sdwa v77, sext(v62) dst_sel:DWORD dst_unused:UNUSED_PAD src0_sel:BYTE_1
	v_cvt_f32_i32_sdwa v76, sext(v62) dst_sel:DWORD dst_unused:UNUSED_PAD src0_sel:BYTE_0
	v_cvt_f32_i32_sdwa v63, sext(v62) dst_sel:DWORD dst_unused:UNUSED_PAD src0_sel:BYTE_3
	v_cvt_f32_i32_sdwa v62, sext(v62) dst_sel:DWORD dst_unused:UNUSED_PAD src0_sel:BYTE_2
	v_cvt_f32_i32_sdwa v79, sext(v3) dst_sel:DWORD dst_unused:UNUSED_PAD src0_sel:BYTE_1
	v_cvt_f32_i32_sdwa v78, sext(v3) dst_sel:DWORD dst_unused:UNUSED_PAD src0_sel:BYTE_0
	v_cvt_f32_i32_sdwa v81, sext(v3) dst_sel:DWORD dst_unused:UNUSED_PAD src0_sel:BYTE_3
	v_cvt_f32_i32_sdwa v80, sext(v3) dst_sel:DWORD dst_unused:UNUSED_PAD src0_sel:BYTE_2
	v_cvt_f32_i32_sdwa v107, sext(v64) dst_sel:DWORD dst_unused:UNUSED_PAD src0_sel:BYTE_1
	v_cvt_f32_i32_sdwa v106, sext(v64) dst_sel:DWORD dst_unused:UNUSED_PAD src0_sel:BYTE_0
	v_cvt_f32_i32_sdwa v65, sext(v64) dst_sel:DWORD dst_unused:UNUSED_PAD src0_sel:BYTE_3
	v_cvt_f32_i32_sdwa v64, sext(v64) dst_sel:DWORD dst_unused:UNUSED_PAD src0_sel:BYTE_2
	v_cvt_f32_i32_sdwa v109, sext(v17) dst_sel:DWORD dst_unused:UNUSED_PAD src0_sel:BYTE_1
	v_cvt_f32_i32_sdwa v108, sext(v17) dst_sel:DWORD dst_unused:UNUSED_PAD src0_sel:BYTE_0
	v_cvt_f32_i32_sdwa v111, sext(v17) dst_sel:DWORD dst_unused:UNUSED_PAD src0_sel:BYTE_3
	v_cvt_f32_i32_sdwa v110, sext(v17) dst_sel:DWORD dst_unused:UNUSED_PAD src0_sel:BYTE_2
	v_pk_fma_f32 v[56:57], v[102:103], v[64:65], v[56:57] op_sel_hi:[0,1,1]
	v_pk_fma_f32 v[58:59], v[102:103], v[108:109], v[58:59] op_sel_hi:[0,1,1]
	v_pk_fma_f32 v[54:55], v[102:103], v[106:107], v[54:55] op_sel_hi:[0,1,1]
	v_pk_fma_f32 v[60:61], v[102:103], v[110:111], v[60:61] op_sel_hi:[0,1,1]
	v_pk_fma_f32 v[68:69], v[102:103], v[80:81], v[68:69] op_sel_hi:[0,1,1]
	v_pk_fma_f32 v[66:67], v[102:103], v[78:79], v[66:67] op_sel_hi:[0,1,1]
	v_pk_fma_f32 v[52:53], v[102:103], v[62:63], v[52:53] op_sel_hi:[0,1,1]
	v_pk_fma_f32 v[50:51], v[102:103], v[76:77], v[50:51] op_sel_hi:[0,1,1]
.LBB0_709:
	s_and_b64 vcc, exec, s[6:7]
	s_cbranch_vccnz .LBB0_711
	v_mov_b32_e32 v62, v208
	v_mov_b32_e32 v3, v209
	v_mov_b32_e32 v64, v210
	v_mov_b32_e32 v17, v211
	v_permlane32_swap_b32_e32 v62, v3
	s_nop 0
	v_permlane32_swap_b32_e32 v64, v17
	v_cvt_f32_i32_sdwa v77, sext(v62) dst_sel:DWORD dst_unused:UNUSED_PAD src0_sel:BYTE_1
	v_cvt_f32_i32_sdwa v76, sext(v62) dst_sel:DWORD dst_unused:UNUSED_PAD src0_sel:BYTE_0
	v_cvt_f32_i32_sdwa v63, sext(v62) dst_sel:DWORD dst_unused:UNUSED_PAD src0_sel:BYTE_3
	v_cvt_f32_i32_sdwa v62, sext(v62) dst_sel:DWORD dst_unused:UNUSED_PAD src0_sel:BYTE_2
	v_cvt_f32_i32_sdwa v79, sext(v3) dst_sel:DWORD dst_unused:UNUSED_PAD src0_sel:BYTE_1
	v_cvt_f32_i32_sdwa v78, sext(v3) dst_sel:DWORD dst_unused:UNUSED_PAD src0_sel:BYTE_0
	v_cvt_f32_i32_sdwa v81, sext(v3) dst_sel:DWORD dst_unused:UNUSED_PAD src0_sel:BYTE_3
	v_cvt_f32_i32_sdwa v80, sext(v3) dst_sel:DWORD dst_unused:UNUSED_PAD src0_sel:BYTE_2
	v_cvt_f32_i32_sdwa v107, sext(v64) dst_sel:DWORD dst_unused:UNUSED_PAD src0_sel:BYTE_1
	v_cvt_f32_i32_sdwa v106, sext(v64) dst_sel:DWORD dst_unused:UNUSED_PAD src0_sel:BYTE_0
	v_cvt_f32_i32_sdwa v65, sext(v64) dst_sel:DWORD dst_unused:UNUSED_PAD src0_sel:BYTE_3
	v_cvt_f32_i32_sdwa v64, sext(v64) dst_sel:DWORD dst_unused:UNUSED_PAD src0_sel:BYTE_2
	v_cvt_f32_i32_sdwa v109, sext(v17) dst_sel:DWORD dst_unused:UNUSED_PAD src0_sel:BYTE_1
	v_cvt_f32_i32_sdwa v108, sext(v17) dst_sel:DWORD dst_unused:UNUSED_PAD src0_sel:BYTE_0
	v_cvt_f32_i32_sdwa v111, sext(v17) dst_sel:DWORD dst_unused:UNUSED_PAD src0_sel:BYTE_3
	v_cvt_f32_i32_sdwa v110, sext(v17) dst_sel:DWORD dst_unused:UNUSED_PAD src0_sel:BYTE_2
	v_pk_fma_f32 v[56:57], v[16:17], v[64:65], v[56:57] op_sel_hi:[0,1,1]
	v_pk_fma_f32 v[58:59], v[16:17], v[108:109], v[58:59] op_sel_hi:[0,1,1]
	v_pk_fma_f32 v[54:55], v[16:17], v[106:107], v[54:55] op_sel_hi:[0,1,1]
	v_pk_fma_f32 v[60:61], v[16:17], v[110:111], v[60:61] op_sel_hi:[0,1,1]
	v_pk_fma_f32 v[68:69], v[16:17], v[80:81], v[68:69] op_sel_hi:[0,1,1]
	v_pk_fma_f32 v[66:67], v[16:17], v[78:79], v[66:67] op_sel_hi:[0,1,1]
	v_pk_fma_f32 v[52:53], v[16:17], v[62:63], v[52:53] op_sel_hi:[0,1,1]
	v_pk_fma_f32 v[50:51], v[16:17], v[76:77], v[50:51] op_sel_hi:[0,1,1]

.LBB0_715:
	s_or_b64 exec, exec, s[10:11]
	v_pk_mul_f32 v[34:35], v[34:35], v[104:105]
	v_pk_mul_f32 v[36:37], v[36:37], v[104:105]
	v_pk_mul_f32 v[50:51], v[38:39], v[104:105]
	v_pk_mul_f32 v[52:53], v[40:41], v[104:105]
	v_pk_mul_f32 v[38:39], v[42:43], v[104:105]
	v_pk_mul_f32 v[40:41], v[44:45], v[104:105]
	v_pk_mul_f32 v[42:43], v[46:47], v[104:105]
	s_and_b64 vcc, exec, s[8:9]
	v_pk_mul_f32 v[44:45], v[48:49], v[104:105]
	s_cbranch_vccnz .LBB0_717
	v_mov_b32_e32 v46, v174
	v_mov_b32_e32 v3, v175
	v_mov_b32_e32 v48, v176
	v_mov_b32_e32 v17, v177
	v_permlane32_swap_b32_e32 v46, v3
	s_nop 0
	v_permlane32_swap_b32_e32 v48, v17
	v_cvt_f32_i32_sdwa v55, sext(v46) dst_sel:DWORD dst_unused:UNUSED_PAD src0_sel:BYTE_1
	v_cvt_f32_i32_sdwa v54, sext(v46) dst_sel:DWORD dst_unused:UNUSED_PAD src0_sel:BYTE_0
	v_cvt_f32_i32_sdwa v47, sext(v46) dst_sel:DWORD dst_unused:UNUSED_PAD src0_sel:BYTE_3
	v_cvt_f32_i32_sdwa v46, sext(v46) dst_sel:DWORD dst_unused:UNUSED_PAD src0_sel:BYTE_2
	v_cvt_f32_i32_sdwa v57, sext(v3) dst_sel:DWORD dst_unused:UNUSED_PAD src0_sel:BYTE_1
	v_cvt_f32_i32_sdwa v56, sext(v3) dst_sel:DWORD dst_unused:UNUSED_PAD src0_sel:BYTE_0
	v_cvt_f32_i32_sdwa v59, sext(v3) dst_sel:DWORD dst_unused:UNUSED_PAD src0_sel:BYTE_3
	v_cvt_f32_i32_sdwa v58, sext(v3) dst_sel:DWORD dst_unused:UNUSED_PAD src0_sel:BYTE_2
	v_cvt_f32_i32_sdwa v61, sext(v48) dst_sel:DWORD dst_unused:UNUSED_PAD src0_sel:BYTE_1
	v_cvt_f32_i32_sdwa v60, sext(v48) dst_sel:DWORD dst_unused:UNUSED_PAD src0_sel:BYTE_0
	v_cvt_f32_i32_sdwa v49, sext(v48) dst_sel:DWORD dst_unused:UNUSED_PAD src0_sel:BYTE_3
	v_cvt_f32_i32_sdwa v48, sext(v48) dst_sel:DWORD dst_unused:UNUSED_PAD src0_sel:BYTE_2
	v_cvt_f32_i32_sdwa v63, sext(v17) dst_sel:DWORD dst_unused:UNUSED_PAD src0_sel:BYTE_1
	v_cvt_f32_i32_sdwa v62, sext(v17) dst_sel:DWORD dst_unused:UNUSED_PAD src0_sel:BYTE_0
	v_cvt_f32_i32_sdwa v65, sext(v17) dst_sel:DWORD dst_unused:UNUSED_PAD src0_sel:BYTE_3
	v_cvt_f32_i32_sdwa v64, sext(v17) dst_sel:DWORD dst_unused:UNUSED_PAD src0_sel:BYTE_2
	v_pk_fma_f32 v[40:41], v[102:103], v[48:49], v[40:41] op_sel_hi:[0,1,1]
	v_pk_fma_f32 v[42:43], v[102:103], v[62:63], v[42:43] op_sel_hi:[0,1,1]
	v_pk_fma_f32 v[38:39], v[102:103], v[60:61], v[38:39] op_sel_hi:[0,1,1]
	v_pk_fma_f32 v[44:45], v[102:103], v[64:65], v[44:45] op_sel_hi:[0,1,1]
	v_pk_fma_f32 v[52:53], v[102:103], v[58:59], v[52:53] op_sel_hi:[0,1,1]
	v_pk_fma_f32 v[50:51], v[102:103], v[56:57], v[50:51] op_sel_hi:[0,1,1]
	v_pk_fma_f32 v[36:37], v[102:103], v[46:47], v[36:37] op_sel_hi:[0,1,1]
	v_pk_fma_f32 v[34:35], v[102:103], v[54:55], v[34:35] op_sel_hi:[0,1,1]
.LBB0_717:
	s_and_b64 vcc, exec, s[6:7]
	s_cbranch_vccnz .LBB0_719
	v_mov_b32_e32 v46, v212
	v_mov_b32_e32 v3, v213
	v_mov_b32_e32 v48, v214
	v_mov_b32_e32 v17, v215
	v_permlane32_swap_b32_e32 v46, v3
	s_nop 0
	v_permlane32_swap_b32_e32 v48, v17
	v_cvt_f32_i32_sdwa v55, sext(v46) dst_sel:DWORD dst_unused:UNUSED_PAD src0_sel:BYTE_1
	v_cvt_f32_i32_sdwa v54, sext(v46) dst_sel:DWORD dst_unused:UNUSED_PAD src0_sel:BYTE_0
	v_cvt_f32_i32_sdwa v47, sext(v46) dst_sel:DWORD dst_unused:UNUSED_PAD src0_sel:BYTE_3
	v_cvt_f32_i32_sdwa v46, sext(v46) dst_sel:DWORD dst_unused:UNUSED_PAD src0_sel:BYTE_2
	v_cvt_f32_i32_sdwa v57, sext(v3) dst_sel:DWORD dst_unused:UNUSED_PAD src0_sel:BYTE_1
	v_cvt_f32_i32_sdwa v56, sext(v3) dst_sel:DWORD dst_unused:UNUSED_PAD src0_sel:BYTE_0
	v_cvt_f32_i32_sdwa v59, sext(v3) dst_sel:DWORD dst_unused:UNUSED_PAD src0_sel:BYTE_3
	v_cvt_f32_i32_sdwa v58, sext(v3) dst_sel:DWORD dst_unused:UNUSED_PAD src0_sel:BYTE_2
	v_cvt_f32_i32_sdwa v61, sext(v48) dst_sel:DWORD dst_unused:UNUSED_PAD src0_sel:BYTE_1
	v_cvt_f32_i32_sdwa v60, sext(v48) dst_sel:DWORD dst_unused:UNUSED_PAD src0_sel:BYTE_0
	v_cvt_f32_i32_sdwa v49, sext(v48) dst_sel:DWORD dst_unused:UNUSED_PAD src0_sel:BYTE_3
	v_cvt_f32_i32_sdwa v48, sext(v48) dst_sel:DWORD dst_unused:UNUSED_PAD src0_sel:BYTE_2
	v_cvt_f32_i32_sdwa v63, sext(v17) dst_sel:DWORD dst_unused:UNUSED_PAD src0_sel:BYTE_1
	v_cvt_f32_i32_sdwa v62, sext(v17) dst_sel:DWORD dst_unused:UNUSED_PAD src0_sel:BYTE_0
	v_cvt_f32_i32_sdwa v65, sext(v17) dst_sel:DWORD dst_unused:UNUSED_PAD src0_sel:BYTE_3
	v_cvt_f32_i32_sdwa v64, sext(v17) dst_sel:DWORD dst_unused:UNUSED_PAD src0_sel:BYTE_2
	v_pk_fma_f32 v[40:41], v[16:17], v[48:49], v[40:41] op_sel_hi:[0,1,1]
	v_pk_fma_f32 v[42:43], v[16:17], v[62:63], v[42:43] op_sel_hi:[0,1,1]
	v_pk_fma_f32 v[38:39], v[16:17], v[60:61], v[38:39] op_sel_hi:[0,1,1]
	v_pk_fma_f32 v[44:45], v[16:17], v[64:65], v[44:45] op_sel_hi:[0,1,1]
	v_pk_fma_f32 v[52:53], v[16:17], v[58:59], v[52:53] op_sel_hi:[0,1,1]
	v_pk_fma_f32 v[50:51], v[16:17], v[56:57], v[50:51] op_sel_hi:[0,1,1]
	v_pk_fma_f32 v[36:37], v[16:17], v[46:47], v[36:37] op_sel_hi:[0,1,1]
	v_pk_fma_f32 v[34:35], v[16:17], v[54:55], v[34:35] op_sel_hi:[0,1,1]

.LBB0_723:
	s_or_b64 exec, exec, s[10:11]
	v_pk_mul_f32 v[18:19], v[18:19], v[104:105]
	v_pk_mul_f32 v[34:35], v[20:21], v[104:105]
	v_pk_mul_f32 v[36:37], v[22:23], v[104:105]
	v_pk_mul_f32 v[38:39], v[24:25], v[104:105]
	v_pk_mul_f32 v[20:21], v[26:27], v[104:105]
	v_pk_mul_f32 v[22:23], v[28:29], v[104:105]
	v_pk_mul_f32 v[24:25], v[30:31], v[104:105]
	s_and_b64 vcc, exec, s[8:9]
	v_pk_mul_f32 v[26:27], v[32:33], v[104:105]
	s_cbranch_vccnz .LBB0_725
	v_mov_b32_e32 v28, v200
	v_mov_b32_e32 v3, v201
	v_mov_b32_e32 v30, v202
	v_mov_b32_e32 v17, v203
	v_permlane32_swap_b32_e32 v28, v3
	s_nop 0
	v_permlane32_swap_b32_e32 v30, v17
	v_cvt_f32_i32_sdwa v33, sext(v28) dst_sel:DWORD dst_unused:UNUSED_PAD src0_sel:BYTE_1
	v_cvt_f32_i32_sdwa v32, sext(v28) dst_sel:DWORD dst_unused:UNUSED_PAD src0_sel:BYTE_0
	v_cvt_f32_i32_sdwa v29, sext(v28) dst_sel:DWORD dst_unused:UNUSED_PAD src0_sel:BYTE_3
	v_cvt_f32_i32_sdwa v28, sext(v28) dst_sel:DWORD dst_unused:UNUSED_PAD src0_sel:BYTE_2
	v_cvt_f32_i32_sdwa v41, sext(v3) dst_sel:DWORD dst_unused:UNUSED_PAD src0_sel:BYTE_1
	v_cvt_f32_i32_sdwa v40, sext(v3) dst_sel:DWORD dst_unused:UNUSED_PAD src0_sel:BYTE_0
	v_cvt_f32_i32_sdwa v43, sext(v3) dst_sel:DWORD dst_unused:UNUSED_PAD src0_sel:BYTE_3
	v_cvt_f32_i32_sdwa v42, sext(v3) dst_sel:DWORD dst_unused:UNUSED_PAD src0_sel:BYTE_2
	v_cvt_f32_i32_sdwa v45, sext(v30) dst_sel:DWORD dst_unused:UNUSED_PAD src0_sel:BYTE_1
	v_cvt_f32_i32_sdwa v44, sext(v30) dst_sel:DWORD dst_unused:UNUSED_PAD src0_sel:BYTE_0
	v_cvt_f32_i32_sdwa v31, sext(v30) dst_sel:DWORD dst_unused:UNUSED_PAD src0_sel:BYTE_3
	v_cvt_f32_i32_sdwa v30, sext(v30) dst_sel:DWORD dst_unused:UNUSED_PAD src0_sel:BYTE_2
	v_cvt_f32_i32_sdwa v47, sext(v17) dst_sel:DWORD dst_unused:UNUSED_PAD src0_sel:BYTE_1
	v_cvt_f32_i32_sdwa v46, sext(v17) dst_sel:DWORD dst_unused:UNUSED_PAD src0_sel:BYTE_0
	v_cvt_f32_i32_sdwa v49, sext(v17) dst_sel:DWORD dst_unused:UNUSED_PAD src0_sel:BYTE_3
	v_cvt_f32_i32_sdwa v48, sext(v17) dst_sel:DWORD dst_unused:UNUSED_PAD src0_sel:BYTE_2
	v_pk_fma_f32 v[22:23], v[102:103], v[30:31], v[22:23] op_sel_hi:[0,1,1]
	v_pk_fma_f32 v[24:25], v[102:103], v[46:47], v[24:25] op_sel_hi:[0,1,1]
	v_pk_fma_f32 v[20:21], v[102:103], v[44:45], v[20:21] op_sel_hi:[0,1,1]
	v_pk_fma_f32 v[26:27], v[102:103], v[48:49], v[26:27] op_sel_hi:[0,1,1]
	v_pk_fma_f32 v[38:39], v[102:103], v[42:43], v[38:39] op_sel_hi:[0,1,1]
	v_pk_fma_f32 v[36:37], v[102:103], v[40:41], v[36:37] op_sel_hi:[0,1,1]
	v_pk_fma_f32 v[34:35], v[102:103], v[28:29], v[34:35] op_sel_hi:[0,1,1]
	v_pk_fma_f32 v[18:19], v[102:103], v[32:33], v[18:19] op_sel_hi:[0,1,1]
.LBB0_725:
	s_and_b64 vcc, exec, s[6:7]
	s_cbranch_vccnz .LBB0_727
	v_mov_b32_e32 v28, v216
	v_mov_b32_e32 v3, v217
	v_mov_b32_e32 v30, v218
	v_mov_b32_e32 v17, v219
	v_permlane32_swap_b32_e32 v28, v3
	s_nop 0
	v_permlane32_swap_b32_e32 v30, v17
	v_cvt_f32_i32_sdwa v33, sext(v28) dst_sel:DWORD dst_unused:UNUSED_PAD src0_sel:BYTE_1
	v_cvt_f32_i32_sdwa v32, sext(v28) dst_sel:DWORD dst_unused:UNUSED_PAD src0_sel:BYTE_0
	v_cvt_f32_i32_sdwa v29, sext(v28) dst_sel:DWORD dst_unused:UNUSED_PAD src0_sel:BYTE_3
	v_cvt_f32_i32_sdwa v28, sext(v28) dst_sel:DWORD dst_unused:UNUSED_PAD src0_sel:BYTE_2
	v_cvt_f32_i32_sdwa v41, sext(v3) dst_sel:DWORD dst_unused:UNUSED_PAD src0_sel:BYTE_1
	v_cvt_f32_i32_sdwa v40, sext(v3) dst_sel:DWORD dst_unused:UNUSED_PAD src0_sel:BYTE_0
	v_cvt_f32_i32_sdwa v43, sext(v3) dst_sel:DWORD dst_unused:UNUSED_PAD src0_sel:BYTE_3
	v_cvt_f32_i32_sdwa v42, sext(v3) dst_sel:DWORD dst_unused:UNUSED_PAD src0_sel:BYTE_2
	v_cvt_f32_i32_sdwa v45, sext(v30) dst_sel:DWORD dst_unused:UNUSED_PAD src0_sel:BYTE_1
	v_cvt_f32_i32_sdwa v44, sext(v30) dst_sel:DWORD dst_unused:UNUSED_PAD src0_sel:BYTE_0
	v_cvt_f32_i32_sdwa v31, sext(v30) dst_sel:DWORD dst_unused:UNUSED_PAD src0_sel:BYTE_3
	v_cvt_f32_i32_sdwa v30, sext(v30) dst_sel:DWORD dst_unused:UNUSED_PAD src0_sel:BYTE_2
	v_cvt_f32_i32_sdwa v47, sext(v17) dst_sel:DWORD dst_unused:UNUSED_PAD src0_sel:BYTE_1
	v_cvt_f32_i32_sdwa v46, sext(v17) dst_sel:DWORD dst_unused:UNUSED_PAD src0_sel:BYTE_0
	v_cvt_f32_i32_sdwa v49, sext(v17) dst_sel:DWORD dst_unused:UNUSED_PAD src0_sel:BYTE_3
	v_cvt_f32_i32_sdwa v48, sext(v17) dst_sel:DWORD dst_unused:UNUSED_PAD src0_sel:BYTE_2
	v_pk_fma_f32 v[22:23], v[16:17], v[30:31], v[22:23] op_sel_hi:[0,1,1]
	v_pk_fma_f32 v[24:25], v[16:17], v[46:47], v[24:25] op_sel_hi:[0,1,1]
	v_pk_fma_f32 v[20:21], v[16:17], v[44:45], v[20:21] op_sel_hi:[0,1,1]
	v_pk_fma_f32 v[26:27], v[16:17], v[48:49], v[26:27] op_sel_hi:[0,1,1]
	v_pk_fma_f32 v[38:39], v[16:17], v[42:43], v[38:39] op_sel_hi:[0,1,1]
	v_pk_fma_f32 v[36:37], v[16:17], v[40:41], v[36:37] op_sel_hi:[0,1,1]
	v_pk_fma_f32 v[34:35], v[16:17], v[28:29], v[34:35] op_sel_hi:[0,1,1]
	v_pk_fma_f32 v[18:19], v[16:17], v[32:33], v[18:19] op_sel_hi:[0,1,1]

.LBB0_753:
	v_cmp_lt_i32_e64 s[74:75], -1, v182
	v_readlane_b32 s6, v255, 25
	v_readlane_b32 s7, v255, 26
	v_readlane_b32 s12, v255, 46
	v_readlane_b32 s13, v255, 47
	v_readlane_b32 s20, v255, 54
	v_readlane_b32 s21, v255, 55
	v_cndmask_b32_e64 v234, 0, v225, s[74:75]
	v_ashrrev_i32_e32 v235, 31, v234
	v_lshl_add_u64 v[238:239], v[234:235], 2, s[6:7]
	global_load_dword v162, v[238:239], off
	v_lshl_add_u64 v[238:239], v[234:235], 2, s[12:13]
	global_load_dword v163, v[238:239], off
	v_lshl_add_u64 v[238:239], v[234:235], 2, s[20:21]
	global_load_dword v164, v[238:239], off
	v_readlane_b32 s6, v255, 29
	v_readlane_b32 s7, v255, 30
	v_readlane_b32 s12, v255, 48
	v_readlane_b32 s13, v255, 49
	v_readlane_b32 s20, v255, 56
	v_readlane_b32 s21, v255, 57
	v_ashrrev_i32_e32 v237, 31, v182
	v_cndmask_b32_e64 v237, 0, v237, s[74:75]
	v_lshl_add_u64 v[238:239], v[234:235], 2, s[6:7]
	global_load_dword v165, v[238:239], off
	v_lshl_add_u64 v[238:239], v[234:235], 2, s[12:13]
	global_load_dword v166, v[238:239], off
	v_lshl_add_u64 v[238:239], v[234:235], 2, s[20:21]
	global_load_dword v167, v[238:239], off
	v_readlane_b32 s6, v255, 41
	v_readlane_b32 s7, v255, 42
	v_and_b32_e32 v236, 0xff800000, v182
	v_bfe_u32 v238, v182, 7, 3
	v_lshl_or_b32 v236, v238, 20, v236
	v_bfe_u32 v238, v182, 10, 13
	v_lshl_or_b32 v236, v238, 7, v236
	v_cndmask_b32_e64 v236, 0, v236, s[74:75]
	v_mov_b32_e32 v237, 0
	v_lshlrev_b32_e32 v238, 3, v179
	v_ashrrev_i32_e32 v239, 31, v238
	v_lshl_add_u64 v[236:237], v[236:237], 0, v[238:239]
	v_lshl_add_u64 v[238:239], s[16:17], 0, v[236:237]
	global_load_dwordx2 v[168:169], v[238:239], off
	global_load_dwordx2 v[170:171], v[238:239], off offset:16
	global_load_dwordx2 v[172:173], v[238:239], off offset:32
	global_load_dwordx2 v[174:175], v[238:239], off offset:48
	global_load_dwordx2 v[176:177], v[238:239], off offset:64
	global_load_dwordx2 v[184:185], v[238:239], off offset:80
	global_load_dwordx2 v[186:187], v[238:239], off offset:96
	global_load_dwordx2 v[188:189], v[238:239], off offset:112
	v_lshl_add_u64 v[238:239], s[6:7], 0, v[236:237]
	global_load_dwordx2 v[190:191], v[238:239], off
	global_load_dwordx2 v[192:193], v[238:239], off offset:16
	global_load_dwordx2 v[194:195], v[238:239], off offset:32
	global_load_dwordx2 v[196:197], v[238:239], off offset:48
	global_load_dwordx2 v[198:199], v[238:239], off offset:64
	global_load_dwordx2 v[200:201], v[238:239], off offset:80
	global_load_dwordx2 v[202:203], v[238:239], off offset:96
	global_load_dwordx2 v[204:205], v[238:239], off offset:112
	v_lshl_add_u64 v[238:239], s[70:71], 0, v[236:237]
	global_load_dwordx2 v[206:207], v[238:239], off
	global_load_dwordx2 v[208:209], v[238:239], off offset:16
	global_load_dwordx2 v[210:211], v[238:239], off offset:32
	global_load_dwordx2 v[212:213], v[238:239], off offset:48
	global_load_dwordx2 v[214:215], v[238:239], off offset:64
	global_load_dwordx2 v[216:217], v[238:239], off offset:80
	global_load_dwordx2 v[230:231], v[238:239], off offset:96
	global_load_dwordx2 v[232:233], v[238:239], off offset:112
	s_waitcnt vmcnt(0)
	v_cmp_lt_i32_e64 s[74:75], -1, v182
	s_cmp_eq_u32 s93, 0
	s_waitcnt vmcnt(3)
	v_mov_b32_e32 v7, 0xff800000
	v_cmp_lt_f32_e64 s[10:11], 0, v218
	v_cndmask_b32_e64 v4, 0, v225, s[74:75]
	s_cselect_b64 s[8:9], -1, 0
	s_cmp_lg_u32 s93, 0
	v_cndmask_b32_e64 v6, v7, v183, s[10:11]
	v_ashrrev_i32_e32 v5, 31, v4
	s_cselect_b64 s[0:1], -1, 0
	s_and_b64 vcc, exec, s[8:9]
	s_cbranch_vccnz .LBB0_755
	v_readlane_b32 s6, v255, 25
	v_readlane_b32 s7, v255, 26
	v_max_f32_e32 v6, v6, v6
	s_waitcnt vmcnt(2)
	v_lshl_add_u64 v[8:9], v[4:5], 2, s[6:7]
	v_mov_b32_e32 v8, v162
	v_max_f32_e32 v3, v8, v8
	v_max_f32_e32 v6, v6, v3
	s_cmp_gt_u32 s93, 1
	s_cselect_b64 s[6:7], -1, 0
	s_cmp_lt_u32 s93, 2
	s_cbranch_scc0 .LBB0_756
	s_branch .LBB0_757

.LBB0_756:
	v_readlane_b32 s12, v255, 46
	v_readlane_b32 s13, v255, 47
	v_max_f32_e32 v6, v6, v6
	s_nop 0
	v_lshl_add_u64 v[10:11], v[4:5], 2, s[12:13]
	v_mov_b32_e32 v7, v163
	v_max_f32_e32 v3, v7, v7
	v_max_f32_e32 v6, v6, v3
.LBB0_757:
	s_cmp_eq_u32 s93, 3
	s_cselect_b64 s[12:13], -1, 0
	s_cmp_lg_u32 s93, 3
	v_mov_b32_e32 v9, 0xff800000
	s_cbranch_scc1 .LBB0_759
	v_readlane_b32 s20, v255, 54
	v_readlane_b32 s21, v255, 55
	v_max_f32_e32 v6, v6, v6
	s_nop 0
	v_lshl_add_u64 v[10:11], v[4:5], 2, s[20:21]
	v_mov_b32_e32 v9, v164
	v_max_f32_e32 v3, v9, v9
	v_max_f32_e32 v6, v6, v3
.LBB0_759:
	v_sub_f32_e32 v3, v183, v6
	v_sub_f32_e32 v10, v8, v6
	v_exp_f32_e32 v3, v3
	v_exp_f32_e32 v10, v10
	s_waitcnt vmcnt(1)
	v_sub_f32_e32 v12, v7, v6
	v_exp_f32_e32 v12, v12
	v_cmp_lg_f32_e32 vcc, s48, v8
	v_sub_f32_e32 v6, v9, v6
	v_cndmask_b32_e64 v3, 0, v3, s[10:11]
	v_cndmask_b32_e32 v10, 0, v10, vcc
	v_exp_f32_e32 v6, v6
	v_mul_f32_e32 v11, v218, v3
	v_cndmask_b32_e64 v8, v10, 0, s[8:9]
	v_fmac_f32_e32 v10, v218, v3
	v_cmp_lg_f32_e32 vcc, s48, v7
	v_cndmask_b32_e64 v10, v10, v11, s[8:9]
	s_nop 0
	v_cndmask_b32_e32 v7, 0, v12, vcc
	v_add_f32_e32 v11, v7, v10
	v_cmp_lg_f32_e32 vcc, s48, v9
	v_cndmask_b32_e64 v10, v10, v11, s[6:7]
	s_nop 0
	v_cndmask_b32_e32 v6, 0, v6, vcc
	v_add_f32_e32 v9, v6, v10
	v_cndmask_b32_e64 v11, v10, v9, s[12:13]
	v_div_scale_f32 v12, s[8:9], v11, v11, 1.0
	v_rcp_f32_e32 v13, v12
	v_cndmask_b32_e64 v9, 0, v7, s[6:7]
	v_mov_b32_e32 v10, 0
	v_cndmask_b32_e64 v6, 0, v6, s[12:13]
	v_fma_f32 v7, -v12, v13, 1.0
	v_fmac_f32_e32 v13, v7, v13
	v_div_scale_f32 v7, vcc, 1.0, v11, 1.0
	v_mul_f32_e32 v14, v7, v13
	v_fma_f32 v15, -v12, v14, v7
	v_fmac_f32_e32 v14, v15, v13
	v_fma_f32 v7, -v12, v14, v7
	v_div_fmas_f32 v7, v7, v13, v14
	v_div_fixup_f32 v7, v7, v11, 1.0
	v_cmp_lt_f32_e32 vcc, 0, v11
	v_cndmask_b32_e64 v11, 0, 1, s[0:1]
	v_cmp_ne_u32_e64 s[10:11], 1, v11
	v_cndmask_b32_e32 v7, 0, v7, vcc
	s_andn2_b64 vcc, exec, s[0:1]
	v_mov_b32_e32 v12, 0
	s_cbranch_vccnz .LBB0_761
	v_readlane_b32 s0, v255, 29
	v_readlane_b32 s1, v255, 30
	v_mul_f32_e32 v8, v8, v7
	s_nop 0
	v_lshl_add_u64 v[12:13], v[4:5], 2, s[0:1]
	v_mov_b32_e32 v11, v165
	v_mul_f32_e32 v12, v8, v11
.LBB0_761:
	v_cndmask_b32_e64 v8, 0, 1, s[6:7]
	v_cmp_ne_u32_e64 s[8:9], 1, v8
	s_andn2_b64 vcc, exec, s[6:7]
	s_cbranch_vccnz .LBB0_763
	v_readlane_b32 s0, v255, 48
	v_readlane_b32 s1, v255, 49
	v_mul_f32_e32 v9, v9, v7
	s_nop 0
	v_lshl_add_u64 v[10:11], v[4:5], 2, s[0:1]
	v_mov_b32_e32 v8, v166
	v_mul_f32_e32 v10, v9, v8
.LBB0_763:
	v_cndmask_b32_e64 v8, 0, 1, s[12:13]
	v_cmp_ne_u32_e64 s[6:7], 1, v8
	s_andn2_b64 vcc, exec, s[12:13]
	v_mov_b32_e32 v8, 0
	s_cbranch_vccnz .LBB0_765
	v_readlane_b32 s0, v255, 56
	v_readlane_b32 s1, v255, 57
	s_nop 1
	v_lshl_add_u64 v[4:5], v[4:5], 2, s[0:1]
	v_mov_b32_e32 v4, v167
	v_mul_f32_e32 v5, v6, v7
	v_mul_f32_e32 v8, v5, v4
.LBB0_765:
	v_ashrrev_i32_e32 v183, 31, v182
	v_cndmask_b32_e64 v89, 0, v183, s[74:75]
	v_cndmask_b32_e64 v88, 0, v182, s[74:75]
	v_lshlrev_b32_e32 v4, 3, v179
	v_mul_f32_e32 v14, v3, v7
	v_ashrrev_i32_e32 v5, 31, v4
	v_lshl_add_u64 v[16:17], s[16:17], 0, v[88:89]
	v_pk_mul_f32 v[6:7], v[66:67], v[14:15] op_sel_hi:[1,0]
	v_pk_mul_f32 v[82:83], v[68:69], v[14:15] op_sel_hi:[1,0]
	v_pk_mul_f32 v[84:85], v[70:71], v[14:15] op_sel_hi:[1,0]
	v_pk_mul_f32 v[86:87], v[72:73], v[14:15] op_sel_hi:[1,0]
	v_pk_mul_f32 v[72:73], v[74:75], v[14:15] op_sel_hi:[1,0]
	v_pk_mul_f32 v[74:75], v[76:77], v[14:15] op_sel_hi:[1,0]
	v_pk_mul_f32 v[76:77], v[78:79], v[14:15] op_sel_hi:[1,0]
	v_pk_mul_f32 v[78:79], v[80:81], v[14:15] op_sel_hi:[1,0]
	s_and_b64 vcc, exec, s[10:11]
	v_lshl_add_u64 v[16:17], v[16:17], 0, v[4:5]
	s_cbranch_vccnz .LBB0_767
	v_mov_b32_e32 v66, v168
	v_mov_b32_e32 v3, v169
	v_mov_b32_e32 v68, v170
	v_mov_b32_e32 v9, v171
	v_permlane32_swap_b32_e32 v66, v3
	s_nop 0
	v_permlane32_swap_b32_e32 v68, v9
	v_cvt_f32_i32_sdwa v71, sext(v66) dst_sel:DWORD dst_unused:UNUSED_PAD src0_sel:BYTE_1
	v_cvt_f32_i32_sdwa v70, sext(v66) dst_sel:DWORD dst_unused:UNUSED_PAD src0_sel:BYTE_0
	v_cvt_f32_i32_sdwa v67, sext(v66) dst_sel:DWORD dst_unused:UNUSED_PAD src0_sel:BYTE_3
	v_cvt_f32_i32_sdwa v66, sext(v66) dst_sel:DWORD dst_unused:UNUSED_PAD src0_sel:BYTE_2
	v_cvt_f32_i32_sdwa v81, sext(v3) dst_sel:DWORD dst_unused:UNUSED_PAD src0_sel:BYTE_1
	v_cvt_f32_i32_sdwa v80, sext(v3) dst_sel:DWORD dst_unused:UNUSED_PAD src0_sel:BYTE_0
	v_cvt_f32_i32_sdwa v91, sext(v3) dst_sel:DWORD dst_unused:UNUSED_PAD src0_sel:BYTE_3
	v_cvt_f32_i32_sdwa v90, sext(v3) dst_sel:DWORD dst_unused:UNUSED_PAD src0_sel:BYTE_2
	v_cvt_f32_i32_sdwa v93, sext(v68) dst_sel:DWORD dst_unused:UNUSED_PAD src0_sel:BYTE_1
	v_cvt_f32_i32_sdwa v92, sext(v68) dst_sel:DWORD dst_unused:UNUSED_PAD src0_sel:BYTE_0
	v_cvt_f32_i32_sdwa v69, sext(v68) dst_sel:DWORD dst_unused:UNUSED_PAD src0_sel:BYTE_3
	v_cvt_f32_i32_sdwa v68, sext(v68) dst_sel:DWORD dst_unused:UNUSED_PAD src0_sel:BYTE_2
	v_cvt_f32_i32_sdwa v95, sext(v9) dst_sel:DWORD dst_unused:UNUSED_PAD src0_sel:BYTE_1
	v_cvt_f32_i32_sdwa v94, sext(v9) dst_sel:DWORD dst_unused:UNUSED_PAD src0_sel:BYTE_0
	v_cvt_f32_i32_sdwa v97, sext(v9) dst_sel:DWORD dst_unused:UNUSED_PAD src0_sel:BYTE_3
	v_cvt_f32_i32_sdwa v96, sext(v9) dst_sel:DWORD dst_unused:UNUSED_PAD src0_sel:BYTE_2
	v_pk_fma_f32 v[74:75], v[12:13], v[68:69], v[74:75] op_sel_hi:[0,1,1]
	v_pk_fma_f32 v[76:77], v[12:13], v[94:95], v[76:77] op_sel_hi:[0,1,1]
	v_pk_fma_f32 v[72:73], v[12:13], v[92:93], v[72:73] op_sel_hi:[0,1,1]
	v_pk_fma_f32 v[78:79], v[12:13], v[96:97], v[78:79] op_sel_hi:[0,1,1]
	v_pk_fma_f32 v[86:87], v[12:13], v[90:91], v[86:87] op_sel_hi:[0,1,1]
	v_pk_fma_f32 v[84:85], v[12:13], v[80:81], v[84:85] op_sel_hi:[0,1,1]
	v_pk_fma_f32 v[82:83], v[12:13], v[66:67], v[82:83] op_sel_hi:[0,1,1]
	v_pk_fma_f32 v[6:7], v[12:13], v[70:71], v[6:7] op_sel_hi:[0,1,1]
.LBB0_767:
	v_readlane_b32 s0, v255, 41
	v_readlane_b32 s1, v255, 42
	s_and_b64 vcc, exec, s[8:9]
	s_nop 0
	v_lshl_add_u64 v[66:67], s[0:1], 0, v[88:89]
	v_lshl_add_u64 v[66:67], v[66:67], 0, v[4:5]
	s_cbranch_vccnz .LBB0_769
	v_mov_b32_e32 v68, v190
	v_mov_b32_e32 v3, v191
	v_mov_b32_e32 v70, v192
	v_mov_b32_e32 v9, v193
	v_permlane32_swap_b32_e32 v68, v3
	s_nop 0
	v_permlane32_swap_b32_e32 v70, v9
	v_cvt_f32_i32_sdwa v81, sext(v68) dst_sel:DWORD dst_unused:UNUSED_PAD src0_sel:BYTE_1
	v_cvt_f32_i32_sdwa v80, sext(v68) dst_sel:DWORD dst_unused:UNUSED_PAD src0_sel:BYTE_0
	v_cvt_f32_i32_sdwa v69, sext(v68) dst_sel:DWORD dst_unused:UNUSED_PAD src0_sel:BYTE_3
	v_cvt_f32_i32_sdwa v68, sext(v68) dst_sel:DWORD dst_unused:UNUSED_PAD src0_sel:BYTE_2
	v_cvt_f32_i32_sdwa v91, sext(v3) dst_sel:DWORD dst_unused:UNUSED_PAD src0_sel:BYTE_1
	v_cvt_f32_i32_sdwa v90, sext(v3) dst_sel:DWORD dst_unused:UNUSED_PAD src0_sel:BYTE_0
	v_cvt_f32_i32_sdwa v93, sext(v3) dst_sel:DWORD dst_unused:UNUSED_PAD src0_sel:BYTE_3
	v_cvt_f32_i32_sdwa v92, sext(v3) dst_sel:DWORD dst_unused:UNUSED_PAD src0_sel:BYTE_2
	v_cvt_f32_i32_sdwa v95, sext(v70) dst_sel:DWORD dst_unused:UNUSED_PAD src0_sel:BYTE_1
	v_cvt_f32_i32_sdwa v94, sext(v70) dst_sel:DWORD dst_unused:UNUSED_PAD src0_sel:BYTE_0
	v_cvt_f32_i32_sdwa v71, sext(v70) dst_sel:DWORD dst_unused:UNUSED_PAD src0_sel:BYTE_3
	v_cvt_f32_i32_sdwa v70, sext(v70) dst_sel:DWORD dst_unused:UNUSED_PAD src0_sel:BYTE_2
	v_cvt_f32_i32_sdwa v97, sext(v9) dst_sel:DWORD dst_unused:UNUSED_PAD src0_sel:BYTE_1
	v_cvt_f32_i32_sdwa v96, sext(v9) dst_sel:DWORD dst_unused:UNUSED_PAD src0_sel:BYTE_0
	v_cvt_f32_i32_sdwa v99, sext(v9) dst_sel:DWORD dst_unused:UNUSED_PAD src0_sel:BYTE_3
	v_cvt_f32_i32_sdwa v98, sext(v9) dst_sel:DWORD dst_unused:UNUSED_PAD src0_sel:BYTE_2
	v_pk_fma_f32 v[74:75], v[10:11], v[70:71], v[74:75] op_sel_hi:[0,1,1]
	v_pk_fma_f32 v[76:77], v[10:11], v[96:97], v[76:77] op_sel_hi:[0,1,1]
	v_pk_fma_f32 v[72:73], v[10:11], v[94:95], v[72:73] op_sel_hi:[0,1,1]
	v_pk_fma_f32 v[78:79], v[10:11], v[98:99], v[78:79] op_sel_hi:[0,1,1]
	v_pk_fma_f32 v[86:87], v[10:11], v[92:93], v[86:87] op_sel_hi:[0,1,1]
	v_pk_fma_f32 v[84:85], v[10:11], v[90:91], v[84:85] op_sel_hi:[0,1,1]
	v_pk_fma_f32 v[82:83], v[10:11], v[68:69], v[82:83] op_sel_hi:[0,1,1]
	v_pk_fma_f32 v[6:7], v[10:11], v[80:81], v[6:7] op_sel_hi:[0,1,1]
.LBB0_769:
	v_lshl_add_u64 v[68:69], s[70:71], 0, v[88:89]
	s_and_b64 vcc, exec, s[6:7]
	v_lshl_add_u64 v[68:69], v[68:69], 0, v[4:5]
	s_cbranch_vccnz .LBB0_771
	v_mov_b32_e32 v70, v206
	v_mov_b32_e32 v3, v207
	v_mov_b32_e32 v80, v208
	v_mov_b32_e32 v9, v209
	v_permlane32_swap_b32_e32 v70, v3
	s_nop 0
	v_permlane32_swap_b32_e32 v80, v9
	v_cvt_f32_i32_sdwa v89, sext(v70) dst_sel:DWORD dst_unused:UNUSED_PAD src0_sel:BYTE_1
	v_cvt_f32_i32_sdwa v88, sext(v70) dst_sel:DWORD dst_unused:UNUSED_PAD src0_sel:BYTE_0
	v_cvt_f32_i32_sdwa v71, sext(v70) dst_sel:DWORD dst_unused:UNUSED_PAD src0_sel:BYTE_3
	v_cvt_f32_i32_sdwa v70, sext(v70) dst_sel:DWORD dst_unused:UNUSED_PAD src0_sel:BYTE_2
	v_cvt_f32_i32_sdwa v91, sext(v3) dst_sel:DWORD dst_unused:UNUSED_PAD src0_sel:BYTE_1
	v_cvt_f32_i32_sdwa v90, sext(v3) dst_sel:DWORD dst_unused:UNUSED_PAD src0_sel:BYTE_0
	v_cvt_f32_i32_sdwa v93, sext(v3) dst_sel:DWORD dst_unused:UNUSED_PAD src0_sel:BYTE_3
	v_cvt_f32_i32_sdwa v92, sext(v3) dst_sel:DWORD dst_unused:UNUSED_PAD src0_sel:BYTE_2
	v_cvt_f32_i32_sdwa v95, sext(v80) dst_sel:DWORD dst_unused:UNUSED_PAD src0_sel:BYTE_1
	v_cvt_f32_i32_sdwa v94, sext(v80) dst_sel:DWORD dst_unused:UNUSED_PAD src0_sel:BYTE_0
	v_cvt_f32_i32_sdwa v81, sext(v80) dst_sel:DWORD dst_unused:UNUSED_PAD src0_sel:BYTE_3
	v_cvt_f32_i32_sdwa v80, sext(v80) dst_sel:DWORD dst_unused:UNUSED_PAD src0_sel:BYTE_2
	v_cvt_f32_i32_sdwa v97, sext(v9) dst_sel:DWORD dst_unused:UNUSED_PAD src0_sel:BYTE_1
	v_cvt_f32_i32_sdwa v96, sext(v9) dst_sel:DWORD dst_unused:UNUSED_PAD src0_sel:BYTE_0
	v_cvt_f32_i32_sdwa v99, sext(v9) dst_sel:DWORD dst_unused:UNUSED_PAD src0_sel:BYTE_3
	v_cvt_f32_i32_sdwa v98, sext(v9) dst_sel:DWORD dst_unused:UNUSED_PAD src0_sel:BYTE_2
	v_pk_fma_f32 v[74:75], v[8:9], v[80:81], v[74:75] op_sel_hi:[0,1,1]
	v_pk_fma_f32 v[76:77], v[8:9], v[96:97], v[76:77] op_sel_hi:[0,1,1]
	v_pk_fma_f32 v[72:73], v[8:9], v[94:95], v[72:73] op_sel_hi:[0,1,1]
	v_pk_fma_f32 v[78:79], v[8:9], v[98:99], v[78:79] op_sel_hi:[0,1,1]
	v_pk_fma_f32 v[86:87], v[8:9], v[92:93], v[86:87] op_sel_hi:[0,1,1]
	v_pk_fma_f32 v[84:85], v[8:9], v[90:91], v[84:85] op_sel_hi:[0,1,1]
	v_pk_fma_f32 v[82:83], v[8:9], v[70:71], v[82:83] op_sel_hi:[0,1,1]
	v_pk_fma_f32 v[6:7], v[8:9], v[88:89], v[6:7] op_sel_hi:[0,1,1]

.LBB0_778:
	v_mov_b32_e32 v58, v210
	v_mov_b32_e32 v3, v211
	v_mov_b32_e32 v60, v212
	v_mov_b32_e32 v9, v213
	v_permlane32_swap_b32_e32 v58, v3
	s_nop 0
	v_permlane32_swap_b32_e32 v60, v9
	v_cvt_f32_i32_sdwa v63, sext(v58) dst_sel:DWORD dst_unused:UNUSED_PAD src0_sel:BYTE_1
	v_cvt_f32_i32_sdwa v62, sext(v58) dst_sel:DWORD dst_unused:UNUSED_PAD src0_sel:BYTE_0
	v_cvt_f32_i32_sdwa v59, sext(v58) dst_sel:DWORD dst_unused:UNUSED_PAD src0_sel:BYTE_3
	v_cvt_f32_i32_sdwa v58, sext(v58) dst_sel:DWORD dst_unused:UNUSED_PAD src0_sel:BYTE_2
	v_cvt_f32_i32_sdwa v65, sext(v3) dst_sel:DWORD dst_unused:UNUSED_PAD src0_sel:BYTE_1
	v_cvt_f32_i32_sdwa v64, sext(v3) dst_sel:DWORD dst_unused:UNUSED_PAD src0_sel:BYTE_0
	v_cvt_f32_i32_sdwa v77, sext(v3) dst_sel:DWORD dst_unused:UNUSED_PAD src0_sel:BYTE_3
	v_cvt_f32_i32_sdwa v76, sext(v3) dst_sel:DWORD dst_unused:UNUSED_PAD src0_sel:BYTE_2
	v_cvt_f32_i32_sdwa v79, sext(v60) dst_sel:DWORD dst_unused:UNUSED_PAD src0_sel:BYTE_1
	v_cvt_f32_i32_sdwa v78, sext(v60) dst_sel:DWORD dst_unused:UNUSED_PAD src0_sel:BYTE_0
	v_cvt_f32_i32_sdwa v61, sext(v60) dst_sel:DWORD dst_unused:UNUSED_PAD src0_sel:BYTE_3
	v_cvt_f32_i32_sdwa v60, sext(v60) dst_sel:DWORD dst_unused:UNUSED_PAD src0_sel:BYTE_2
	v_cvt_f32_i32_sdwa v81, sext(v9) dst_sel:DWORD dst_unused:UNUSED_PAD src0_sel:BYTE_1
	v_cvt_f32_i32_sdwa v80, sext(v9) dst_sel:DWORD dst_unused:UNUSED_PAD src0_sel:BYTE_0
	v_cvt_f32_i32_sdwa v83, sext(v9) dst_sel:DWORD dst_unused:UNUSED_PAD src0_sel:BYTE_3
	v_cvt_f32_i32_sdwa v82, sext(v9) dst_sel:DWORD dst_unused:UNUSED_PAD src0_sel:BYTE_2
	v_pk_fma_f32 v[52:53], v[8:9], v[60:61], v[52:53] op_sel_hi:[0,1,1]
	v_pk_fma_f32 v[54:55], v[8:9], v[80:81], v[54:55] op_sel_hi:[0,1,1]
	v_pk_fma_f32 v[50:51], v[8:9], v[78:79], v[50:51] op_sel_hi:[0,1,1]
	v_pk_fma_f32 v[56:57], v[8:9], v[82:83], v[56:57] op_sel_hi:[0,1,1]
	v_pk_fma_f32 v[74:75], v[8:9], v[76:77], v[74:75] op_sel_hi:[0,1,1]
	v_pk_fma_f32 v[72:73], v[8:9], v[64:65], v[72:73] op_sel_hi:[0,1,1]
	v_pk_fma_f32 v[6:7], v[8:9], v[58:59], v[6:7] op_sel_hi:[0,1,1]
	v_pk_fma_f32 v[4:5], v[8:9], v[62:63], v[4:5] op_sel_hi:[0,1,1]

.LBB0_786:
	v_mov_b32_e32 v42, v214
	v_mov_b32_e32 v3, v215
	v_mov_b32_e32 v44, v216
	v_mov_b32_e32 v9, v217
	v_permlane32_swap_b32_e32 v42, v3
	s_nop 0
	v_permlane32_swap_b32_e32 v44, v9
	v_cvt_f32_i32_sdwa v47, sext(v42) dst_sel:DWORD dst_unused:UNUSED_PAD src0_sel:BYTE_1
	v_cvt_f32_i32_sdwa v46, sext(v42) dst_sel:DWORD dst_unused:UNUSED_PAD src0_sel:BYTE_0
	v_cvt_f32_i32_sdwa v43, sext(v42) dst_sel:DWORD dst_unused:UNUSED_PAD src0_sel:BYTE_3
	v_cvt_f32_i32_sdwa v42, sext(v42) dst_sel:DWORD dst_unused:UNUSED_PAD src0_sel:BYTE_2
	v_cvt_f32_i32_sdwa v49, sext(v3) dst_sel:DWORD dst_unused:UNUSED_PAD src0_sel:BYTE_1
	v_cvt_f32_i32_sdwa v48, sext(v3) dst_sel:DWORD dst_unused:UNUSED_PAD src0_sel:BYTE_0
	v_cvt_f32_i32_sdwa v55, sext(v3) dst_sel:DWORD dst_unused:UNUSED_PAD src0_sel:BYTE_3
	v_cvt_f32_i32_sdwa v54, sext(v3) dst_sel:DWORD dst_unused:UNUSED_PAD src0_sel:BYTE_2
	v_cvt_f32_i32_sdwa v57, sext(v44) dst_sel:DWORD dst_unused:UNUSED_PAD src0_sel:BYTE_1
	v_cvt_f32_i32_sdwa v56, sext(v44) dst_sel:DWORD dst_unused:UNUSED_PAD src0_sel:BYTE_0
	v_cvt_f32_i32_sdwa v45, sext(v44) dst_sel:DWORD dst_unused:UNUSED_PAD src0_sel:BYTE_3
	v_cvt_f32_i32_sdwa v44, sext(v44) dst_sel:DWORD dst_unused:UNUSED_PAD src0_sel:BYTE_2
	v_cvt_f32_i32_sdwa v59, sext(v9) dst_sel:DWORD dst_unused:UNUSED_PAD src0_sel:BYTE_1
	v_cvt_f32_i32_sdwa v58, sext(v9) dst_sel:DWORD dst_unused:UNUSED_PAD src0_sel:BYTE_0
	v_cvt_f32_i32_sdwa v61, sext(v9) dst_sel:DWORD dst_unused:UNUSED_PAD src0_sel:BYTE_3
	v_cvt_f32_i32_sdwa v60, sext(v9) dst_sel:DWORD dst_unused:UNUSED_PAD src0_sel:BYTE_2
	v_pk_fma_f32 v[36:37], v[8:9], v[44:45], v[36:37] op_sel_hi:[0,1,1]
	v_pk_fma_f32 v[38:39], v[8:9], v[58:59], v[38:39] op_sel_hi:[0,1,1]
	v_pk_fma_f32 v[34:35], v[8:9], v[56:57], v[34:35] op_sel_hi:[0,1,1]
	v_pk_fma_f32 v[40:41], v[8:9], v[60:61], v[40:41] op_sel_hi:[0,1,1]
	v_pk_fma_f32 v[52:53], v[8:9], v[54:55], v[52:53] op_sel_hi:[0,1,1]
	v_pk_fma_f32 v[50:51], v[8:9], v[48:49], v[50:51] op_sel_hi:[0,1,1]
	v_pk_fma_f32 v[6:7], v[8:9], v[42:43], v[6:7] op_sel_hi:[0,1,1]
	v_pk_fma_f32 v[4:5], v[8:9], v[46:47], v[4:5] op_sel_hi:[0,1,1]

.LBB0_794:
	v_mov_b32_e32 v10, v230
	v_mov_b32_e32 v3, v231
	v_mov_b32_e32 v12, v232
	v_mov_b32_e32 v9, v233
	v_permlane32_swap_b32_e32 v10, v3
	s_nop 0
	v_permlane32_swap_b32_e32 v12, v9
	v_cvt_f32_i32_sdwa v17, sext(v10) dst_sel:DWORD dst_unused:UNUSED_PAD src0_sel:BYTE_1
	v_cvt_f32_i32_sdwa v16, sext(v10) dst_sel:DWORD dst_unused:UNUSED_PAD src0_sel:BYTE_0
	v_cvt_f32_i32_sdwa v11, sext(v10) dst_sel:DWORD dst_unused:UNUSED_PAD src0_sel:BYTE_3
	v_cvt_f32_i32_sdwa v10, sext(v10) dst_sel:DWORD dst_unused:UNUSED_PAD src0_sel:BYTE_2
	v_cvt_f32_i32_sdwa v27, sext(v3) dst_sel:DWORD dst_unused:UNUSED_PAD src0_sel:BYTE_1
	v_cvt_f32_i32_sdwa v26, sext(v3) dst_sel:DWORD dst_unused:UNUSED_PAD src0_sel:BYTE_0
	v_cvt_f32_i32_sdwa v29, sext(v3) dst_sel:DWORD dst_unused:UNUSED_PAD src0_sel:BYTE_3
	v_cvt_f32_i32_sdwa v28, sext(v3) dst_sel:DWORD dst_unused:UNUSED_PAD src0_sel:BYTE_2
	v_cvt_f32_i32_sdwa v31, sext(v12) dst_sel:DWORD dst_unused:UNUSED_PAD src0_sel:BYTE_1
	v_cvt_f32_i32_sdwa v30, sext(v12) dst_sel:DWORD dst_unused:UNUSED_PAD src0_sel:BYTE_0
	v_cvt_f32_i32_sdwa v13, sext(v12) dst_sel:DWORD dst_unused:UNUSED_PAD src0_sel:BYTE_3
	v_cvt_f32_i32_sdwa v12, sext(v12) dst_sel:DWORD dst_unused:UNUSED_PAD src0_sel:BYTE_2
	v_cvt_f32_i32_sdwa v33, sext(v9) dst_sel:DWORD dst_unused:UNUSED_PAD src0_sel:BYTE_1
	v_cvt_f32_i32_sdwa v32, sext(v9) dst_sel:DWORD dst_unused:UNUSED_PAD src0_sel:BYTE_0
	v_cvt_f32_i32_sdwa v37, sext(v9) dst_sel:DWORD dst_unused:UNUSED_PAD src0_sel:BYTE_3
	v_cvt_f32_i32_sdwa v36, sext(v9) dst_sel:DWORD dst_unused:UNUSED_PAD src0_sel:BYTE_2
	v_pk_fma_f32 v[20:21], v[8:9], v[12:13], v[20:21] op_sel_hi:[0,1,1]
	v_pk_fma_f32 v[22:23], v[8:9], v[32:33], v[22:23] op_sel_hi:[0,1,1]
	v_pk_fma_f32 v[18:19], v[8:9], v[30:31], v[18:19] op_sel_hi:[0,1,1]
	v_pk_fma_f32 v[14:15], v[8:9], v[36:37], v[14:15] op_sel_hi:[0,1,1]
	v_pk_fma_f32 v[24:25], v[8:9], v[28:29], v[24:25] op_sel_hi:[0,1,1]
	v_pk_fma_f32 v[34:35], v[8:9], v[26:27], v[34:35] op_sel_hi:[0,1,1]
	v_pk_fma_f32 v[6:7], v[8:9], v[10:11], v[6:7] op_sel_hi:[0,1,1]
	v_pk_fma_f32 v[4:5], v[8:9], v[16:17], v[4:5] op_sel_hi:[0,1,1]

.LBB0_800:
	v_mov_b32_e32 v58, v172
	v_mov_b32_e32 v3, v173
	v_mov_b32_e32 v60, v174
	v_mov_b32_e32 v9, v175
	v_permlane32_swap_b32_e32 v58, v3
	s_nop 0
	v_permlane32_swap_b32_e32 v60, v9
	v_cvt_f32_i32_sdwa v63, sext(v58) dst_sel:DWORD dst_unused:UNUSED_PAD src0_sel:BYTE_1
	v_cvt_f32_i32_sdwa v62, sext(v58) dst_sel:DWORD dst_unused:UNUSED_PAD src0_sel:BYTE_0
	v_cvt_f32_i32_sdwa v59, sext(v58) dst_sel:DWORD dst_unused:UNUSED_PAD src0_sel:BYTE_3
	v_cvt_f32_i32_sdwa v58, sext(v58) dst_sel:DWORD dst_unused:UNUSED_PAD src0_sel:BYTE_2
	v_cvt_f32_i32_sdwa v65, sext(v3) dst_sel:DWORD dst_unused:UNUSED_PAD src0_sel:BYTE_1
	v_cvt_f32_i32_sdwa v64, sext(v3) dst_sel:DWORD dst_unused:UNUSED_PAD src0_sel:BYTE_0
	v_cvt_f32_i32_sdwa v77, sext(v3) dst_sel:DWORD dst_unused:UNUSED_PAD src0_sel:BYTE_3
	v_cvt_f32_i32_sdwa v76, sext(v3) dst_sel:DWORD dst_unused:UNUSED_PAD src0_sel:BYTE_2
	v_cvt_f32_i32_sdwa v79, sext(v60) dst_sel:DWORD dst_unused:UNUSED_PAD src0_sel:BYTE_1
	v_cvt_f32_i32_sdwa v78, sext(v60) dst_sel:DWORD dst_unused:UNUSED_PAD src0_sel:BYTE_0
	v_cvt_f32_i32_sdwa v61, sext(v60) dst_sel:DWORD dst_unused:UNUSED_PAD src0_sel:BYTE_3
	v_cvt_f32_i32_sdwa v60, sext(v60) dst_sel:DWORD dst_unused:UNUSED_PAD src0_sel:BYTE_2
	v_cvt_f32_i32_sdwa v81, sext(v9) dst_sel:DWORD dst_unused:UNUSED_PAD src0_sel:BYTE_1
	v_cvt_f32_i32_sdwa v80, sext(v9) dst_sel:DWORD dst_unused:UNUSED_PAD src0_sel:BYTE_0
	v_cvt_f32_i32_sdwa v83, sext(v9) dst_sel:DWORD dst_unused:UNUSED_PAD src0_sel:BYTE_3
	v_cvt_f32_i32_sdwa v82, sext(v9) dst_sel:DWORD dst_unused:UNUSED_PAD src0_sel:BYTE_2
	v_pk_fma_f32 v[52:53], v[12:13], v[60:61], v[52:53] op_sel_hi:[0,1,1]
	v_pk_fma_f32 v[54:55], v[12:13], v[80:81], v[54:55] op_sel_hi:[0,1,1]
	v_pk_fma_f32 v[50:51], v[12:13], v[78:79], v[50:51] op_sel_hi:[0,1,1]
	v_pk_fma_f32 v[56:57], v[12:13], v[82:83], v[56:57] op_sel_hi:[0,1,1]
	v_pk_fma_f32 v[74:75], v[12:13], v[76:77], v[74:75] op_sel_hi:[0,1,1]
	v_pk_fma_f32 v[72:73], v[12:13], v[64:65], v[72:73] op_sel_hi:[0,1,1]
	v_pk_fma_f32 v[6:7], v[12:13], v[58:59], v[6:7] op_sel_hi:[0,1,1]
	v_pk_fma_f32 v[4:5], v[12:13], v[62:63], v[4:5] op_sel_hi:[0,1,1]
	s_and_b64 vcc, exec, s[8:9]
	s_cbranch_vccnz .LBB0_777
.LBB0_801:
	v_mov_b32_e32 v58, v194
	v_mov_b32_e32 v3, v195
	v_mov_b32_e32 v60, v196
	v_mov_b32_e32 v9, v197
	v_permlane32_swap_b32_e32 v58, v3
	s_nop 0
	v_permlane32_swap_b32_e32 v60, v9
	v_cvt_f32_i32_sdwa v63, sext(v58) dst_sel:DWORD dst_unused:UNUSED_PAD src0_sel:BYTE_1
	v_cvt_f32_i32_sdwa v62, sext(v58) dst_sel:DWORD dst_unused:UNUSED_PAD src0_sel:BYTE_0
	v_cvt_f32_i32_sdwa v59, sext(v58) dst_sel:DWORD dst_unused:UNUSED_PAD src0_sel:BYTE_3
	v_cvt_f32_i32_sdwa v58, sext(v58) dst_sel:DWORD dst_unused:UNUSED_PAD src0_sel:BYTE_2
	v_cvt_f32_i32_sdwa v65, sext(v3) dst_sel:DWORD dst_unused:UNUSED_PAD src0_sel:BYTE_1
	v_cvt_f32_i32_sdwa v64, sext(v3) dst_sel:DWORD dst_unused:UNUSED_PAD src0_sel:BYTE_0
	v_cvt_f32_i32_sdwa v77, sext(v3) dst_sel:DWORD dst_unused:UNUSED_PAD src0_sel:BYTE_3
	v_cvt_f32_i32_sdwa v76, sext(v3) dst_sel:DWORD dst_unused:UNUSED_PAD src0_sel:BYTE_2
	v_cvt_f32_i32_sdwa v79, sext(v60) dst_sel:DWORD dst_unused:UNUSED_PAD src0_sel:BYTE_1
	v_cvt_f32_i32_sdwa v78, sext(v60) dst_sel:DWORD dst_unused:UNUSED_PAD src0_sel:BYTE_0
	v_cvt_f32_i32_sdwa v61, sext(v60) dst_sel:DWORD dst_unused:UNUSED_PAD src0_sel:BYTE_3
	v_cvt_f32_i32_sdwa v60, sext(v60) dst_sel:DWORD dst_unused:UNUSED_PAD src0_sel:BYTE_2
	v_cvt_f32_i32_sdwa v81, sext(v9) dst_sel:DWORD dst_unused:UNUSED_PAD src0_sel:BYTE_1
	v_cvt_f32_i32_sdwa v80, sext(v9) dst_sel:DWORD dst_unused:UNUSED_PAD src0_sel:BYTE_0
	v_cvt_f32_i32_sdwa v83, sext(v9) dst_sel:DWORD dst_unused:UNUSED_PAD src0_sel:BYTE_3
	v_cvt_f32_i32_sdwa v82, sext(v9) dst_sel:DWORD dst_unused:UNUSED_PAD src0_sel:BYTE_2
	v_pk_fma_f32 v[52:53], v[10:11], v[60:61], v[52:53] op_sel_hi:[0,1,1]
	v_pk_fma_f32 v[54:55], v[10:11], v[80:81], v[54:55] op_sel_hi:[0,1,1]
	v_pk_fma_f32 v[50:51], v[10:11], v[78:79], v[50:51] op_sel_hi:[0,1,1]
	v_pk_fma_f32 v[56:57], v[10:11], v[82:83], v[56:57] op_sel_hi:[0,1,1]
	v_pk_fma_f32 v[74:75], v[10:11], v[76:77], v[74:75] op_sel_hi:[0,1,1]
	v_pk_fma_f32 v[72:73], v[10:11], v[64:65], v[72:73] op_sel_hi:[0,1,1]
	v_pk_fma_f32 v[6:7], v[10:11], v[58:59], v[6:7] op_sel_hi:[0,1,1]
	v_pk_fma_f32 v[4:5], v[10:11], v[62:63], v[4:5] op_sel_hi:[0,1,1]
	s_and_b64 vcc, exec, s[6:7]
	s_cbranch_vccz .LBB0_778
	s_branch .LBB0_779
.LBB0_802:
	v_mov_b32_e32 v42, v176
	v_mov_b32_e32 v3, v177
	v_mov_b32_e32 v44, v184
	v_mov_b32_e32 v9, v185
	v_permlane32_swap_b32_e32 v42, v3
	s_nop 0
	v_permlane32_swap_b32_e32 v44, v9
	v_cvt_f32_i32_sdwa v47, sext(v42) dst_sel:DWORD dst_unused:UNUSED_PAD src0_sel:BYTE_1
	v_cvt_f32_i32_sdwa v46, sext(v42) dst_sel:DWORD dst_unused:UNUSED_PAD src0_sel:BYTE_0
	v_cvt_f32_i32_sdwa v43, sext(v42) dst_sel:DWORD dst_unused:UNUSED_PAD src0_sel:BYTE_3
	v_cvt_f32_i32_sdwa v42, sext(v42) dst_sel:DWORD dst_unused:UNUSED_PAD src0_sel:BYTE_2
	v_cvt_f32_i32_sdwa v49, sext(v3) dst_sel:DWORD dst_unused:UNUSED_PAD src0_sel:BYTE_1
	v_cvt_f32_i32_sdwa v48, sext(v3) dst_sel:DWORD dst_unused:UNUSED_PAD src0_sel:BYTE_0
	v_cvt_f32_i32_sdwa v55, sext(v3) dst_sel:DWORD dst_unused:UNUSED_PAD src0_sel:BYTE_3
	v_cvt_f32_i32_sdwa v54, sext(v3) dst_sel:DWORD dst_unused:UNUSED_PAD src0_sel:BYTE_2
	v_cvt_f32_i32_sdwa v57, sext(v44) dst_sel:DWORD dst_unused:UNUSED_PAD src0_sel:BYTE_1
	v_cvt_f32_i32_sdwa v56, sext(v44) dst_sel:DWORD dst_unused:UNUSED_PAD src0_sel:BYTE_0
	v_cvt_f32_i32_sdwa v45, sext(v44) dst_sel:DWORD dst_unused:UNUSED_PAD src0_sel:BYTE_3
	v_cvt_f32_i32_sdwa v44, sext(v44) dst_sel:DWORD dst_unused:UNUSED_PAD src0_sel:BYTE_2
	v_cvt_f32_i32_sdwa v59, sext(v9) dst_sel:DWORD dst_unused:UNUSED_PAD src0_sel:BYTE_1
	v_cvt_f32_i32_sdwa v58, sext(v9) dst_sel:DWORD dst_unused:UNUSED_PAD src0_sel:BYTE_0
	v_cvt_f32_i32_sdwa v61, sext(v9) dst_sel:DWORD dst_unused:UNUSED_PAD src0_sel:BYTE_3
	v_cvt_f32_i32_sdwa v60, sext(v9) dst_sel:DWORD dst_unused:UNUSED_PAD src0_sel:BYTE_2
	v_pk_fma_f32 v[36:37], v[12:13], v[44:45], v[36:37] op_sel_hi:[0,1,1]
	v_pk_fma_f32 v[38:39], v[12:13], v[58:59], v[38:39] op_sel_hi:[0,1,1]
	v_pk_fma_f32 v[34:35], v[12:13], v[56:57], v[34:35] op_sel_hi:[0,1,1]
	v_pk_fma_f32 v[40:41], v[12:13], v[60:61], v[40:41] op_sel_hi:[0,1,1]
	v_pk_fma_f32 v[52:53], v[12:13], v[54:55], v[52:53] op_sel_hi:[0,1,1]
	v_pk_fma_f32 v[50:51], v[12:13], v[48:49], v[50:51] op_sel_hi:[0,1,1]
	v_pk_fma_f32 v[6:7], v[12:13], v[42:43], v[6:7] op_sel_hi:[0,1,1]
	v_pk_fma_f32 v[4:5], v[12:13], v[46:47], v[4:5] op_sel_hi:[0,1,1]
	s_and_b64 vcc, exec, s[8:9]
	s_cbranch_vccnz .LBB0_785
.LBB0_803:
	v_mov_b32_e32 v42, v198
	v_mov_b32_e32 v3, v199
	v_mov_b32_e32 v44, v200
	v_mov_b32_e32 v9, v201
	v_permlane32_swap_b32_e32 v42, v3
	s_nop 0
	v_permlane32_swap_b32_e32 v44, v9
	v_cvt_f32_i32_sdwa v47, sext(v42) dst_sel:DWORD dst_unused:UNUSED_PAD src0_sel:BYTE_1
	v_cvt_f32_i32_sdwa v46, sext(v42) dst_sel:DWORD dst_unused:UNUSED_PAD src0_sel:BYTE_0
	v_cvt_f32_i32_sdwa v43, sext(v42) dst_sel:DWORD dst_unused:UNUSED_PAD src0_sel:BYTE_3
	v_cvt_f32_i32_sdwa v42, sext(v42) dst_sel:DWORD dst_unused:UNUSED_PAD src0_sel:BYTE_2
	v_cvt_f32_i32_sdwa v49, sext(v3) dst_sel:DWORD dst_unused:UNUSED_PAD src0_sel:BYTE_1
	v_cvt_f32_i32_sdwa v48, sext(v3) dst_sel:DWORD dst_unused:UNUSED_PAD src0_sel:BYTE_0
	v_cvt_f32_i32_sdwa v55, sext(v3) dst_sel:DWORD dst_unused:UNUSED_PAD src0_sel:BYTE_3
	v_cvt_f32_i32_sdwa v54, sext(v3) dst_sel:DWORD dst_unused:UNUSED_PAD src0_sel:BYTE_2
	v_cvt_f32_i32_sdwa v57, sext(v44) dst_sel:DWORD dst_unused:UNUSED_PAD src0_sel:BYTE_1
	v_cvt_f32_i32_sdwa v56, sext(v44) dst_sel:DWORD dst_unused:UNUSED_PAD src0_sel:BYTE_0
	v_cvt_f32_i32_sdwa v45, sext(v44) dst_sel:DWORD dst_unused:UNUSED_PAD src0_sel:BYTE_3
	v_cvt_f32_i32_sdwa v44, sext(v44) dst_sel:DWORD dst_unused:UNUSED_PAD src0_sel:BYTE_2
	v_cvt_f32_i32_sdwa v59, sext(v9) dst_sel:DWORD dst_unused:UNUSED_PAD src0_sel:BYTE_1
	v_cvt_f32_i32_sdwa v58, sext(v9) dst_sel:DWORD dst_unused:UNUSED_PAD src0_sel:BYTE_0
	v_cvt_f32_i32_sdwa v61, sext(v9) dst_sel:DWORD dst_unused:UNUSED_PAD src0_sel:BYTE_3
	v_cvt_f32_i32_sdwa v60, sext(v9) dst_sel:DWORD dst_unused:UNUSED_PAD src0_sel:BYTE_2
	v_pk_fma_f32 v[36:37], v[10:11], v[44:45], v[36:37] op_sel_hi:[0,1,1]
	v_pk_fma_f32 v[38:39], v[10:11], v[58:59], v[38:39] op_sel_hi:[0,1,1]
	v_pk_fma_f32 v[34:35], v[10:11], v[56:57], v[34:35] op_sel_hi:[0,1,1]
	v_pk_fma_f32 v[40:41], v[10:11], v[60:61], v[40:41] op_sel_hi:[0,1,1]
	v_pk_fma_f32 v[52:53], v[10:11], v[54:55], v[52:53] op_sel_hi:[0,1,1]
	v_pk_fma_f32 v[50:51], v[10:11], v[48:49], v[50:51] op_sel_hi:[0,1,1]
	v_pk_fma_f32 v[6:7], v[10:11], v[42:43], v[6:7] op_sel_hi:[0,1,1]
	v_pk_fma_f32 v[4:5], v[10:11], v[46:47], v[4:5] op_sel_hi:[0,1,1]
	s_and_b64 vcc, exec, s[6:7]
	s_cbranch_vccz .LBB0_786
	s_branch .LBB0_787
.LBB0_804:
	v_mov_b32_e32 v26, v186
	v_mov_b32_e32 v3, v187
	v_mov_b32_e32 v16, v188
	v_mov_b32_e32 v17, v189
	s_nop 0
	v_permlane32_swap_b32_e32 v26, v3
	v_cvt_f32_i32_sdwa v29, sext(v26) dst_sel:DWORD dst_unused:UNUSED_PAD src0_sel:BYTE_1
	v_cvt_f32_i32_sdwa v28, sext(v26) dst_sel:DWORD dst_unused:UNUSED_PAD src0_sel:BYTE_0
	v_cvt_f32_i32_sdwa v27, sext(v26) dst_sel:DWORD dst_unused:UNUSED_PAD src0_sel:BYTE_3
	v_cvt_f32_i32_sdwa v26, sext(v26) dst_sel:DWORD dst_unused:UNUSED_PAD src0_sel:BYTE_2
	v_cvt_f32_i32_sdwa v31, sext(v3) dst_sel:DWORD dst_unused:UNUSED_PAD src0_sel:BYTE_1
	v_cvt_f32_i32_sdwa v30, sext(v3) dst_sel:DWORD dst_unused:UNUSED_PAD src0_sel:BYTE_0
	v_cvt_f32_i32_sdwa v33, sext(v3) dst_sel:DWORD dst_unused:UNUSED_PAD src0_sel:BYTE_3
	v_cvt_f32_i32_sdwa v32, sext(v3) dst_sel:DWORD dst_unused:UNUSED_PAD src0_sel:BYTE_2
	v_pk_fma_f32 v[6:7], v[12:13], v[26:27], v[6:7] op_sel_hi:[0,1,1]
	v_pk_fma_f32 v[34:35], v[12:13], v[30:31], v[34:35] op_sel_hi:[0,1,1]
	v_pk_fma_f32 v[4:5], v[12:13], v[28:29], v[4:5] op_sel_hi:[0,1,1]
	v_pk_fma_f32 v[24:25], v[12:13], v[32:33], v[24:25] op_sel_hi:[0,1,1]
	v_mov_b32_e32 v9, v17
	s_nop 1
	v_permlane32_swap_b32_e32 v16, v9
	v_cvt_f32_i32_sdwa v37, sext(v16) dst_sel:DWORD dst_unused:UNUSED_PAD src0_sel:BYTE_1
	v_cvt_f32_i32_sdwa v36, sext(v16) dst_sel:DWORD dst_unused:UNUSED_PAD src0_sel:BYTE_0
	v_cvt_f32_i32_sdwa v17, sext(v16) dst_sel:DWORD dst_unused:UNUSED_PAD src0_sel:BYTE_3
	v_cvt_f32_i32_sdwa v16, sext(v16) dst_sel:DWORD dst_unused:UNUSED_PAD src0_sel:BYTE_2
	v_cvt_f32_i32_sdwa v39, sext(v9) dst_sel:DWORD dst_unused:UNUSED_PAD src0_sel:BYTE_1
	v_cvt_f32_i32_sdwa v38, sext(v9) dst_sel:DWORD dst_unused:UNUSED_PAD src0_sel:BYTE_0
	v_cvt_f32_i32_sdwa v41, sext(v9) dst_sel:DWORD dst_unused:UNUSED_PAD src0_sel:BYTE_3
	v_cvt_f32_i32_sdwa v40, sext(v9) dst_sel:DWORD dst_unused:UNUSED_PAD src0_sel:BYTE_2
	v_pk_fma_f32 v[20:21], v[12:13], v[16:17], v[20:21] op_sel_hi:[0,1,1]
	v_pk_fma_f32 v[22:23], v[12:13], v[38:39], v[22:23] op_sel_hi:[0,1,1]
	v_pk_fma_f32 v[18:19], v[12:13], v[36:37], v[18:19] op_sel_hi:[0,1,1]
	v_pk_fma_f32 v[14:15], v[12:13], v[40:41], v[14:15] op_sel_hi:[0,1,1]
	s_and_b64 vcc, exec, s[8:9]
	s_cbranch_vccnz .LBB0_793
.LBB0_805:
	v_mov_b32_e32 v12, v202
	v_mov_b32_e32 v3, v203
	v_mov_b32_e32 v16, v204
	v_mov_b32_e32 v9, v205
	v_permlane32_swap_b32_e32 v12, v3
	s_nop 0
	v_permlane32_swap_b32_e32 v16, v9
	v_cvt_f32_i32_sdwa v27, sext(v12) dst_sel:DWORD dst_unused:UNUSED_PAD src0_sel:BYTE_1
	v_cvt_f32_i32_sdwa v26, sext(v12) dst_sel:DWORD dst_unused:UNUSED_PAD src0_sel:BYTE_0
	v_cvt_f32_i32_sdwa v13, sext(v12) dst_sel:DWORD dst_unused:UNUSED_PAD src0_sel:BYTE_3
	v_cvt_f32_i32_sdwa v12, sext(v12) dst_sel:DWORD dst_unused:UNUSED_PAD src0_sel:BYTE_2
	v_cvt_f32_i32_sdwa v29, sext(v3) dst_sel:DWORD dst_unused:UNUSED_PAD src0_sel:BYTE_1
	v_cvt_f32_i32_sdwa v28, sext(v3) dst_sel:DWORD dst_unused:UNUSED_PAD src0_sel:BYTE_0
	v_cvt_f32_i32_sdwa v31, sext(v3) dst_sel:DWORD dst_unused:UNUSED_PAD src0_sel:BYTE_3
	v_cvt_f32_i32_sdwa v30, sext(v3) dst_sel:DWORD dst_unused:UNUSED_PAD src0_sel:BYTE_2
	v_cvt_f32_i32_sdwa v33, sext(v16) dst_sel:DWORD dst_unused:UNUSED_PAD src0_sel:BYTE_1
	v_cvt_f32_i32_sdwa v32, sext(v16) dst_sel:DWORD dst_unused:UNUSED_PAD src0_sel:BYTE_0
	v_cvt_f32_i32_sdwa v17, sext(v16) dst_sel:DWORD dst_unused:UNUSED_PAD src0_sel:BYTE_3
	v_cvt_f32_i32_sdwa v16, sext(v16) dst_sel:DWORD dst_unused:UNUSED_PAD src0_sel:BYTE_2
	v_cvt_f32_i32_sdwa v37, sext(v9) dst_sel:DWORD dst_unused:UNUSED_PAD src0_sel:BYTE_1
	v_cvt_f32_i32_sdwa v36, sext(v9) dst_sel:DWORD dst_unused:UNUSED_PAD src0_sel:BYTE_0
	v_cvt_f32_i32_sdwa v39, sext(v9) dst_sel:DWORD dst_unused:UNUSED_PAD src0_sel:BYTE_3
	v_cvt_f32_i32_sdwa v38, sext(v9) dst_sel:DWORD dst_unused:UNUSED_PAD src0_sel:BYTE_2
	v_pk_fma_f32 v[20:21], v[10:11], v[16:17], v[20:21] op_sel_hi:[0,1,1]
	v_pk_fma_f32 v[22:23], v[10:11], v[36:37], v[22:23] op_sel_hi:[0,1,1]
	v_pk_fma_f32 v[18:19], v[10:11], v[32:33], v[18:19] op_sel_hi:[0,1,1]
	v_pk_fma_f32 v[14:15], v[10:11], v[38:39], v[14:15] op_sel_hi:[0,1,1]
	v_pk_fma_f32 v[24:25], v[10:11], v[30:31], v[24:25] op_sel_hi:[0,1,1]
	v_pk_fma_f32 v[34:35], v[10:11], v[28:29], v[34:35] op_sel_hi:[0,1,1]
	v_pk_fma_f32 v[6:7], v[10:11], v[12:13], v[6:7] op_sel_hi:[0,1,1]
	v_pk_fma_f32 v[4:5], v[10:11], v[26:27], v[4:5] op_sel_hi:[0,1,1]
	s_and_b64 vcc, exec, s[6:7]
	s_cbranch_vccz .LBB0_794
	s_branch .LBB0_795

.LBB0_1298:
	s_cmp_lt_i32 s92, 12
	s_cselect_b64 s[8:9], -1, 0
	s_add_u32 s20, s26, 0x39c0000
	s_addc_u32 s21, s27, 0
	s_add_u32 s0, s26, 0x3a00000
	s_addc_u32 s1, s27, 0
	s_add_u32 s50, s26, 0x3a80000
	s_addc_u32 s51, s27, 0
	s_and_b64 s[10:11], s[8:9], s[6:7]
	s_andn2_b64 vcc, exec, s[10:11]
	s_cbranch_vccnz .LBB0_1326
	v_mov_b32_e32 v1, v254
	s_waitcnt vmcnt(0)
	v_add_u32_e32 v6, s86, v1
	v_cmp_eq_u32_e32 vcc, 0, v6
	s_barrier
	s_and_saveexec_b64 s[6:7], vcc
	s_cbranch_execz .LBB0_1301
	v_mov_b32_e32 v2, 0x48000
	v_mov_b32_e32 v4, 0x49000
	global_load_dword v7, v2, s[26:27] sc1
	global_load_dword v8, v2, s[26:27] offset:256 sc1
	global_load_dword v9, v2, s[26:27] offset:512 sc1
	global_load_dword v10, v2, s[26:27] offset:768 sc1
	global_load_dword v11, v2, s[26:27] offset:1024 sc1
	global_load_dword v12, v2, s[26:27] offset:1280 sc1
	global_load_dword v13, v2, s[26:27] offset:1536 sc1
	global_load_dword v14, v2, s[26:27] offset:1792 sc1
	global_load_dword v15, v2, s[26:27] offset:2048 sc1
	global_load_dword v16, v2, s[26:27] offset:2304 sc1
	global_load_dword v17, v2, s[26:27] offset:2560 sc1
	global_load_dword v18, v2, s[26:27] offset:2816 sc1
	global_load_dword v19, v2, s[26:27] offset:3072 sc1
	global_load_dword v20, v2, s[26:27] offset:3328 sc1
	global_load_dword v21, v2, s[26:27] offset:3584 sc1
	global_load_dword v22, v2, s[26:27] offset:3840 sc1
	global_load_dword v23, v4, s[26:27] sc1
	global_load_dword v24, v4, s[26:27] offset:256 sc1
	global_load_dword v25, v4, s[26:27] offset:512 sc1
	global_load_dword v26, v4, s[26:27] offset:768 sc1
	global_load_dword v27, v4, s[26:27] offset:1024 sc1
	global_load_dword v28, v4, s[26:27] offset:1280 sc1
	global_load_dword v29, v4, s[26:27] offset:1536 sc1
	global_load_dword v30, v4, s[26:27] offset:1792 sc1
	global_load_dword v31, v4, s[26:27] offset:2048 sc1
	global_load_dword v32, v4, s[26:27] offset:2304 sc1
	global_load_dword v33, v4, s[26:27] offset:2560 sc1
	global_load_dword v34, v4, s[26:27] offset:2816 sc1
	global_load_dword v35, v4, s[26:27] offset:3072 sc1
	global_load_dword v36, v4, s[26:27] offset:3328 sc1
	global_load_dword v37, v4, s[26:27] offset:3584 sc1
	global_load_dword v38, v4, s[26:27] offset:3840 sc1
	s_mov_b32 s2, 0x1fc00
	v_mov_b32_e32 v3, s2
	v_mov_b32_e32 v5, 0
	ds_write_b32 v3, v5
	s_waitcnt vmcnt(0)
	v_add_u32_e32 v7, 0xff, v7
	v_and_b32_e32 v7, 0xffffff00, v7
	ds_write_b32 v3, v7 offset:4
	v_add_u32_e32 v8, 0xff, v8
	v_and_b32_e32 v8, 0xffffff00, v8
	v_add_u32_e32 v8, v8, v7
	ds_write_b32 v3, v8 offset:8
	v_add_u32_e32 v9, 0xff, v9
	v_and_b32_e32 v9, 0xffffff00, v9
	v_add_u32_e32 v9, v9, v8
	ds_write_b32 v3, v9 offset:12
	v_add_u32_e32 v10, 0xff, v10
	v_and_b32_e32 v10, 0xffffff00, v10
	v_add_u32_e32 v10, v10, v9
	ds_write_b32 v3, v10 offset:16
	v_add_u32_e32 v11, 0xff, v11
	v_and_b32_e32 v11, 0xffffff00, v11
	v_add_u32_e32 v11, v11, v10
	ds_write_b32 v3, v11 offset:20
	v_add_u32_e32 v12, 0xff, v12
	v_and_b32_e32 v12, 0xffffff00, v12
	v_add_u32_e32 v12, v12, v11
	ds_write_b32 v3, v12 offset:24
	v_add_u32_e32 v13, 0xff, v13
	v_and_b32_e32 v13, 0xffffff00, v13
	v_add_u32_e32 v13, v13, v12
	ds_write_b32 v3, v13 offset:28
	v_add_u32_e32 v14, 0xff, v14
	v_and_b32_e32 v14, 0xffffff00, v14
	v_add_u32_e32 v14, v14, v13
	ds_write_b32 v3, v14 offset:32
	v_add_u32_e32 v15, 0xff, v15
	v_and_b32_e32 v15, 0xffffff00, v15
	v_add_u32_e32 v15, v15, v14
	ds_write_b32 v3, v15 offset:36
	v_add_u32_e32 v16, 0xff, v16
	v_and_b32_e32 v16, 0xffffff00, v16
	v_add_u32_e32 v16, v16, v15
	ds_write_b32 v3, v16 offset:40
	v_add_u32_e32 v17, 0xff, v17
	v_and_b32_e32 v17, 0xffffff00, v17
	v_add_u32_e32 v17, v17, v16
	ds_write_b32 v3, v17 offset:44
	v_add_u32_e32 v18, 0xff, v18
	v_and_b32_e32 v18, 0xffffff00, v18
	v_add_u32_e32 v18, v18, v17
	ds_write_b32 v3, v18 offset:48
	v_add_u32_e32 v19, 0xff, v19
	v_and_b32_e32 v19, 0xffffff00, v19
	v_add_u32_e32 v19, v19, v18
	ds_write_b32 v3, v19 offset:52
	v_add_u32_e32 v20, 0xff, v20
	v_and_b32_e32 v20, 0xffffff00, v20
	v_add_u32_e32 v20, v20, v19
	ds_write_b32 v3, v20 offset:56
	v_add_u32_e32 v21, 0xff, v21
	v_and_b32_e32 v21, 0xffffff00, v21
	v_add_u32_e32 v21, v21, v20
	ds_write_b32 v3, v21 offset:60
	v_add_u32_e32 v22, 0xff, v22
	v_and_b32_e32 v22, 0xffffff00, v22
	v_add_u32_e32 v22, v22, v21
	ds_write_b32 v3, v22 offset:64
	v_add_u32_e32 v23, 0xff, v23
	v_and_b32_e32 v23, 0xffffff00, v23
	v_add_u32_e32 v23, v23, v22
	ds_write_b32 v3, v23 offset:68
	v_add_u32_e32 v24, 0xff, v24
	v_and_b32_e32 v24, 0xffffff00, v24
	v_add_u32_e32 v24, v24, v23
	ds_write_b32 v3, v24 offset:72
	v_add_u32_e32 v25, 0xff, v25
	v_and_b32_e32 v25, 0xffffff00, v25
	v_add_u32_e32 v25, v25, v24
	ds_write_b32 v3, v25 offset:76
	v_add_u32_e32 v26, 0xff, v26
	v_and_b32_e32 v26, 0xffffff00, v26
	v_add_u32_e32 v26, v26, v25
	ds_write_b32 v3, v26 offset:80
	v_add_u32_e32 v27, 0xff, v27
	v_and_b32_e32 v27, 0xffffff00, v27
	v_add_u32_e32 v27, v27, v26
	ds_write_b32 v3, v27 offset:84
	v_add_u32_e32 v28, 0xff, v28
	v_and_b32_e32 v28, 0xffffff00, v28
	v_add_u32_e32 v28, v28, v27
	ds_write_b32 v3, v28 offset:88
	v_add_u32_e32 v29, 0xff, v29
	v_and_b32_e32 v29, 0xffffff00, v29
	v_add_u32_e32 v29, v29, v28
	ds_write_b32 v3, v29 offset:92
	v_add_u32_e32 v30, 0xff, v30
	v_and_b32_e32 v30, 0xffffff00, v30
	v_add_u32_e32 v30, v30, v29
	ds_write_b32 v3, v30 offset:96
	v_add_u32_e32 v31, 0xff, v31
	v_and_b32_e32 v31, 0xffffff00, v31
	v_add_u32_e32 v31, v31, v30
	ds_write_b32 v3, v31 offset:100
	v_add_u32_e32 v32, 0xff, v32
	v_and_b32_e32 v32, 0xffffff00, v32
	v_add_u32_e32 v32, v32, v31
	ds_write_b32 v3, v32 offset:104
	v_add_u32_e32 v33, 0xff, v33
	v_and_b32_e32 v33, 0xffffff00, v33
	v_add_u32_e32 v33, v33, v32
	ds_write_b32 v3, v33 offset:108
	v_add_u32_e32 v34, 0xff, v34
	v_and_b32_e32 v34, 0xffffff00, v34
	v_add_u32_e32 v34, v34, v33
	ds_write_b32 v3, v34 offset:112
	v_add_u32_e32 v35, 0xff, v35
	v_and_b32_e32 v35, 0xffffff00, v35
	v_add_u32_e32 v35, v35, v34
	ds_write_b32 v3, v35 offset:116
	v_add_u32_e32 v36, 0xff, v36
	v_and_b32_e32 v36, 0xffffff00, v36
	v_add_u32_e32 v36, v36, v35
	ds_write_b32 v3, v36 offset:120
	v_add_u32_e32 v37, 0xff, v37
	v_and_b32_e32 v37, 0xffffff00, v37
	v_add_u32_e32 v37, v37, v36
	ds_write_b32 v3, v37 offset:124
	v_add_u32_e32 v38, 0xff, v38
	v_and_b32_e32 v38, 0xffffff00, v38
	v_add_u32_e32 v38, v38, v37
	ds_write_b32 v3, v38 offset:128

.LBB0_1383:
	s_and_b64 vcc, exec, s[4:5]
	s_cbranch_vccz .LBB0_1663
	v_mov_b32_e32 v1, v254
	s_mov_b32 s4, 0
	v_sub_u32_e32 v1, 0, v1
	v_cmp_eq_u32_e32 vcc, s86, v1
	s_waitcnt vmcnt(0)
	s_barrier
	s_and_saveexec_b64 s[6:7], vcc
	s_cbranch_execz .LBB0_1386
	v_mov_b32_e32 v1, 0x48000
	v_mov_b32_e32 v3, 0x49000
	global_load_dword v4, v1, s[26:27] sc1
	global_load_dword v5, v1, s[26:27] offset:256 sc1
	global_load_dword v6, v1, s[26:27] offset:512 sc1
	global_load_dword v7, v1, s[26:27] offset:768 sc1
	global_load_dword v8, v1, s[26:27] offset:1024 sc1
	global_load_dword v9, v1, s[26:27] offset:1280 sc1
	global_load_dword v10, v1, s[26:27] offset:1536 sc1
	global_load_dword v11, v1, s[26:27] offset:1792 sc1
	global_load_dword v12, v1, s[26:27] offset:2048 sc1
	global_load_dword v13, v1, s[26:27] offset:2304 sc1
	global_load_dword v14, v1, s[26:27] offset:2560 sc1
	global_load_dword v15, v1, s[26:27] offset:2816 sc1
	global_load_dword v16, v1, s[26:27] offset:3072 sc1
	global_load_dword v17, v1, s[26:27] offset:3328 sc1
	global_load_dword v18, v1, s[26:27] offset:3584 sc1
	global_load_dword v19, v1, s[26:27] offset:3840 sc1
	global_load_dword v20, v3, s[26:27] sc1
	global_load_dword v21, v3, s[26:27] offset:256 sc1
	global_load_dword v22, v3, s[26:27] offset:512 sc1
	global_load_dword v23, v3, s[26:27] offset:768 sc1
	global_load_dword v24, v3, s[26:27] offset:1024 sc1
	global_load_dword v25, v3, s[26:27] offset:1280 sc1
	global_load_dword v26, v3, s[26:27] offset:1536 sc1
	global_load_dword v27, v3, s[26:27] offset:1792 sc1
	global_load_dword v28, v3, s[26:27] offset:2048 sc1
	global_load_dword v29, v3, s[26:27] offset:2304 sc1
	global_load_dword v30, v3, s[26:27] offset:2560 sc1
	global_load_dword v31, v3, s[26:27] offset:2816 sc1
	global_load_dword v32, v3, s[26:27] offset:3072 sc1
	global_load_dword v33, v3, s[26:27] offset:3328 sc1
	global_load_dword v34, v3, s[26:27] offset:3584 sc1
	global_load_dword v35, v3, s[26:27] offset:3840 sc1
	s_mov_b32 s2, 0x20040
	v_mov_b32_e32 v2, s2
	v_mov_b32_e32 v36, 0
	ds_write_b32 v2, v36
	s_waitcnt vmcnt(0)
	v_add_u32_e32 v4, 0xff, v4
	v_ashrrev_i32_e32 v4, 8, v4
	ds_write_b32 v2, v4 offset:4
	v_add_u32_e32 v5, 0xff, v5
	v_ashrrev_i32_e32 v5, 8, v5
	v_add_u32_e32 v5, v5, v4
	ds_write_b32 v2, v5 offset:8
	v_add_u32_e32 v6, 0xff, v6
	v_ashrrev_i32_e32 v6, 8, v6
	v_add_u32_e32 v6, v6, v5
	ds_write_b32 v2, v6 offset:12
	v_add_u32_e32 v7, 0xff, v7
	v_ashrrev_i32_e32 v7, 8, v7
	v_add_u32_e32 v7, v7, v6
	ds_write_b32 v2, v7 offset:16
	v_add_u32_e32 v8, 0xff, v8
	v_ashrrev_i32_e32 v8, 8, v8
	v_add_u32_e32 v8, v8, v7
	ds_write_b32 v2, v8 offset:20
	v_add_u32_e32 v9, 0xff, v9
	v_ashrrev_i32_e32 v9, 8, v9
	v_add_u32_e32 v9, v9, v8
	ds_write_b32 v2, v9 offset:24
	v_add_u32_e32 v10, 0xff, v10
	v_ashrrev_i32_e32 v10, 8, v10
	v_add_u32_e32 v10, v10, v9
	ds_write_b32 v2, v10 offset:28
	v_add_u32_e32 v11, 0xff, v11
	v_ashrrev_i32_e32 v11, 8, v11
	v_add_u32_e32 v11, v11, v10
	ds_write_b32 v2, v11 offset:32
	v_add_u32_e32 v12, 0xff, v12
	v_ashrrev_i32_e32 v12, 8, v12
	v_add_u32_e32 v12, v12, v11
	ds_write_b32 v2, v12 offset:36
	v_add_u32_e32 v13, 0xff, v13
	v_ashrrev_i32_e32 v13, 8, v13
	v_add_u32_e32 v13, v13, v12
	ds_write_b32 v2, v13 offset:40
	v_add_u32_e32 v14, 0xff, v14
	v_ashrrev_i32_e32 v14, 8, v14
	v_add_u32_e32 v14, v14, v13
	ds_write_b32 v2, v14 offset:44
	v_add_u32_e32 v15, 0xff, v15
	v_ashrrev_i32_e32 v15, 8, v15
	v_add_u32_e32 v15, v15, v14
	ds_write_b32 v2, v15 offset:48
	v_add_u32_e32 v16, 0xff, v16
	v_ashrrev_i32_e32 v16, 8, v16
	v_add_u32_e32 v16, v16, v15
	ds_write_b32 v2, v16 offset:52
	v_add_u32_e32 v17, 0xff, v17
	v_ashrrev_i32_e32 v17, 8, v17
	v_add_u32_e32 v17, v17, v16
	ds_write_b32 v2, v17 offset:56
	v_add_u32_e32 v18, 0xff, v18
	v_ashrrev_i32_e32 v18, 8, v18
	v_add_u32_e32 v18, v18, v17
	ds_write_b32 v2, v18 offset:60
	v_add_u32_e32 v19, 0xff, v19
	v_ashrrev_i32_e32 v19, 8, v19
	v_add_u32_e32 v19, v19, v18
	ds_write_b32 v2, v19 offset:64
	v_add_u32_e32 v20, 0xff, v20
	v_ashrrev_i32_e32 v20, 8, v20
	v_add_u32_e32 v20, v20, v19
	ds_write_b32 v2, v20 offset:68
	v_add_u32_e32 v21, 0xff, v21
	v_ashrrev_i32_e32 v21, 8, v21
	v_add_u32_e32 v21, v21, v20
	ds_write_b32 v2, v21 offset:72
	v_add_u32_e32 v22, 0xff, v22
	v_ashrrev_i32_e32 v22, 8, v22
	v_add_u32_e32 v22, v22, v21
	ds_write_b32 v2, v22 offset:76
	v_add_u32_e32 v23, 0xff, v23
	v_ashrrev_i32_e32 v23, 8, v23
	v_add_u32_e32 v23, v23, v22
	ds_write_b32 v2, v23 offset:80
	v_add_u32_e32 v24, 0xff, v24
	v_ashrrev_i32_e32 v24, 8, v24
	v_add_u32_e32 v24, v24, v23
	ds_write_b32 v2, v24 offset:84
	v_add_u32_e32 v25, 0xff, v25
	v_ashrrev_i32_e32 v25, 8, v25
	v_add_u32_e32 v25, v25, v24
	ds_write_b32 v2, v25 offset:88
	v_add_u32_e32 v26, 0xff, v26
	v_ashrrev_i32_e32 v26, 8, v26
	v_add_u32_e32 v26, v26, v25
	ds_write_b32 v2, v26 offset:92
	v_add_u32_e32 v27, 0xff, v27
	v_ashrrev_i32_e32 v27, 8, v27
	v_add_u32_e32 v27, v27, v26
	ds_write_b32 v2, v27 offset:96
	v_add_u32_e32 v28, 0xff, v28
	v_ashrrev_i32_e32 v28, 8, v28
	v_add_u32_e32 v28, v28, v27
	ds_write_b32 v2, v28 offset:100
	v_add_u32_e32 v29, 0xff, v29
	v_ashrrev_i32_e32 v29, 8, v29
	v_add_u32_e32 v29, v29, v28
	ds_write_b32 v2, v29 offset:104
	v_add_u32_e32 v30, 0xff, v30
	v_ashrrev_i32_e32 v30, 8, v30
	v_add_u32_e32 v30, v30, v29
	ds_write_b32 v2, v30 offset:108
	v_add_u32_e32 v31, 0xff, v31
	v_ashrrev_i32_e32 v31, 8, v31
	v_add_u32_e32 v31, v31, v30
	ds_write_b32 v2, v31 offset:112
	v_add_u32_e32 v32, 0xff, v32
	v_ashrrev_i32_e32 v32, 8, v32
	v_add_u32_e32 v32, v32, v31
	ds_write_b32 v2, v32 offset:116
	v_add_u32_e32 v33, 0xff, v33
	v_ashrrev_i32_e32 v33, 8, v33
	v_add_u32_e32 v33, v33, v32
	ds_write_b32 v2, v33 offset:120
	v_add_u32_e32 v34, 0xff, v34
	v_ashrrev_i32_e32 v34, 8, v34
	v_add_u32_e32 v34, v34, v33
	ds_write_b32 v2, v34 offset:124
	v_add_u32_e32 v35, 0xff, v35
	v_ashrrev_i32_e32 v35, 8, v35
	v_add_u32_e32 v35, v35, v34
	ds_write_b32 v2, v35 offset:128
